# bf16 loops keep 8/6 fragment reads in flight across the phase barrier, fp8 loops 4 late reads; all ds_reads issued first in each LD segment
# speedup vs baseline: 1.0064x; 1.0064x over previous
.LBB0_219:
	s_waitcnt lgkmcnt(0)
	s_add_i32 s4, s92, 0x180
	s_add_i32 s5, s93, 0x180
	s_barrier
	s_setprio 1
	s_waitcnt lgkmcnt(7)
	v_mfma_f32_16x16x32_bf16 v[60:63], v[156:159], v[188:191], 0
	s_waitcnt lgkmcnt(6)
	v_mfma_f32_16x16x32_bf16 v[60:63], v[152:155], v[184:187], v[60:63]
	v_mfma_f32_16x16x32_bf16 v[56:59], v[148:151], v[188:191], 0
	s_nop 0
	v_mfma_f32_16x16x32_bf16 v[56:59], v[144:147], v[184:187], v[56:59]
	s_waitcnt lgkmcnt(5)
	v_mfma_f32_16x16x32_bf16 v[52:55], v[156:159], v[180:183], 0
	s_waitcnt lgkmcnt(4)
	v_mfma_f32_16x16x32_bf16 v[52:55], v[152:155], v[176:179], v[52:55]
	v_mfma_f32_16x16x32_bf16 v[48:51], v[148:151], v[180:183], 0
	s_nop 0
	v_mfma_f32_16x16x32_bf16 v[48:51], v[144:147], v[176:179], v[48:51]
	s_waitcnt lgkmcnt(3)
	v_mfma_f32_16x16x32_bf16 v[44:47], v[156:159], v[172:175], 0
	s_waitcnt lgkmcnt(2)
	v_mfma_f32_16x16x32_bf16 v[44:47], v[152:155], v[168:171], v[44:47]
	v_mfma_f32_16x16x32_bf16 v[40:43], v[148:151], v[172:175], 0
	s_nop 0
	v_mfma_f32_16x16x32_bf16 v[40:43], v[144:147], v[168:171], v[40:43]
	s_waitcnt lgkmcnt(1)
	v_mfma_f32_16x16x32_bf16 v[36:39], v[156:159], v[164:167], 0
	s_waitcnt lgkmcnt(0)
	v_mfma_f32_16x16x32_bf16 v[36:39], v[152:155], v[160:163], v[36:39]
	v_mfma_f32_16x16x32_bf16 v[32:35], v[148:151], v[164:167], 0
	s_nop 0
	v_mfma_f32_16x16x32_bf16 v[32:35], v[144:147], v[160:163], v[32:35]
	s_setprio 0
	s_setprio 1
	v_mfma_f32_16x16x32_bf16 v[28:31], v[140:143], v[188:191], 0
	s_nop 0
	v_mfma_f32_16x16x32_bf16 v[28:31], v[136:139], v[184:187], v[28:31]
	v_mfma_f32_16x16x32_bf16 v[24:27], v[132:135], v[188:191], 0
	s_nop 0
	v_mfma_f32_16x16x32_bf16 v[24:27], v[128:131], v[184:187], v[24:27]
	v_mfma_f32_16x16x32_bf16 v[20:23], v[140:143], v[180:183], 0
	s_nop 0
	v_mfma_f32_16x16x32_bf16 v[20:23], v[136:139], v[176:179], v[20:23]
	v_mfma_f32_16x16x32_bf16 v[16:19], v[132:135], v[180:183], 0
	s_nop 0
	v_mfma_f32_16x16x32_bf16 v[16:19], v[128:131], v[176:179], v[16:19]
	v_mfma_f32_16x16x32_bf16 v[12:15], v[140:143], v[172:175], 0
	s_nop 0
	v_mfma_f32_16x16x32_bf16 v[12:15], v[136:139], v[168:171], v[12:15]
	v_mfma_f32_16x16x32_bf16 v[8:11], v[132:135], v[172:175], 0
	s_nop 0
	v_mfma_f32_16x16x32_bf16 v[8:11], v[128:131], v[168:171], v[8:11]
	v_mfma_f32_16x16x32_bf16 v[4:7], v[140:143], v[164:167], 0
	s_nop 0
	v_mfma_f32_16x16x32_bf16 v[4:7], v[136:139], v[160:163], v[4:7]
	v_mfma_f32_16x16x32_bf16 v[0:3], v[132:135], v[164:167], 0
	s_nop 0
	v_mfma_f32_16x16x32_bf16 v[0:3], v[128:131], v[160:163], v[0:3]
	s_setprio 0
	s_barrier
	ds_read_b128 v[156:159], v211
	ds_read_b128 v[152:155], v212
	ds_read_b128 v[148:151], v213
	ds_read_b128 v[144:147], v214
	ds_read_b128 v[140:143], v215
	ds_read_b128 v[136:139], v216
	ds_read_b128 v[132:135], v217
	ds_read_b128 v[128:131], v218
	ds_read_b128 v[160:163], v219 offset:32768
	ds_read_b128 v[164:167], v219 offset:33792
	ds_read_b128 v[168:171], v219 offset:34816
	ds_read_b128 v[172:175], v219 offset:35840
	ds_read_b128 v[176:179], v219 offset:36864
	ds_read_b128 v[180:183], v219 offset:37888
	ds_read_b128 v[184:187], v219 offset:38912
	ds_read_b128 v[188:191], v219 offset:39936
	s_mov_b32 m0, s69
	s_add_i32 s14, s92, 0x20100
	buffer_load_dwordx4 v196, s[8:11], s14 offen lds
	s_add_i32 s14, s92, 0x30100
	s_mov_b32 m0, s70
	s_nop 0
	buffer_load_dwordx4 v196, s[8:11], s14 offen lds
	s_waitcnt vmcnt(8)
	s_waitcnt lgkmcnt(8)
	s_barrier
	s_setprio 1
	s_waitcnt lgkmcnt(7)
	v_mfma_f32_16x16x32_bf16 v[124:127], v[156:159], v[160:163], v[124:127]
	s_waitcnt lgkmcnt(6)
	v_mfma_f32_16x16x32_bf16 v[124:127], v[152:155], v[164:167], v[124:127]
	v_mfma_f32_16x16x32_bf16 v[120:123], v[148:151], v[160:163], v[120:123]
	s_nop 0
	v_mfma_f32_16x16x32_bf16 v[120:123], v[144:147], v[164:167], v[120:123]
	s_waitcnt lgkmcnt(5)
	v_mfma_f32_16x16x32_bf16 v[116:119], v[156:159], v[168:171], v[116:119]
	s_waitcnt lgkmcnt(4)
	v_mfma_f32_16x16x32_bf16 v[116:119], v[152:155], v[172:175], v[116:119]
	v_mfma_f32_16x16x32_bf16 v[112:115], v[148:151], v[168:171], v[112:115]
	s_nop 0
	v_mfma_f32_16x16x32_bf16 v[112:115], v[144:147], v[172:175], v[112:115]
	s_waitcnt lgkmcnt(3)
	v_mfma_f32_16x16x32_bf16 v[108:111], v[156:159], v[176:179], v[108:111]
	s_waitcnt lgkmcnt(2)
	v_mfma_f32_16x16x32_bf16 v[108:111], v[152:155], v[180:183], v[108:111]
	v_mfma_f32_16x16x32_bf16 v[104:107], v[148:151], v[176:179], v[104:107]
	s_nop 0
	v_mfma_f32_16x16x32_bf16 v[104:107], v[144:147], v[180:183], v[104:107]
	s_waitcnt lgkmcnt(1)
	v_mfma_f32_16x16x32_bf16 v[100:103], v[156:159], v[184:187], v[100:103]
	s_waitcnt lgkmcnt(0)
	v_mfma_f32_16x16x32_bf16 v[100:103], v[152:155], v[188:191], v[100:103]
	v_mfma_f32_16x16x32_bf16 v[96:99], v[148:151], v[184:187], v[96:99]
	s_nop 0
	v_mfma_f32_16x16x32_bf16 v[96:99], v[144:147], v[188:191], v[96:99]
	s_setprio 0
	s_setprio 1
	v_mfma_f32_16x16x32_bf16 v[92:95], v[140:143], v[160:163], v[92:95]
	s_nop 0
	v_mfma_f32_16x16x32_bf16 v[92:95], v[136:139], v[164:167], v[92:95]
	v_mfma_f32_16x16x32_bf16 v[88:91], v[132:135], v[160:163], v[88:91]
	s_nop 0
	v_mfma_f32_16x16x32_bf16 v[88:91], v[128:131], v[164:167], v[88:91]
	v_mfma_f32_16x16x32_bf16 v[84:87], v[140:143], v[168:171], v[84:87]
	s_nop 0
	v_mfma_f32_16x16x32_bf16 v[84:87], v[136:139], v[172:175], v[84:87]
	v_mfma_f32_16x16x32_bf16 v[80:83], v[132:135], v[168:171], v[80:83]
	s_nop 0
	v_mfma_f32_16x16x32_bf16 v[80:83], v[128:131], v[172:175], v[80:83]
	v_mfma_f32_16x16x32_bf16 v[76:79], v[140:143], v[176:179], v[76:79]
	s_nop 0
	v_mfma_f32_16x16x32_bf16 v[76:79], v[136:139], v[180:183], v[76:79]
	v_mfma_f32_16x16x32_bf16 v[72:75], v[132:135], v[176:179], v[72:75]
	s_nop 0
	v_mfma_f32_16x16x32_bf16 v[72:75], v[128:131], v[180:183], v[72:75]
	v_mfma_f32_16x16x32_bf16 v[68:71], v[140:143], v[184:187], v[68:71]
	s_nop 0
	v_mfma_f32_16x16x32_bf16 v[68:71], v[136:139], v[188:191], v[68:71]
	v_mfma_f32_16x16x32_bf16 v[64:67], v[132:135], v[184:187], v[64:67]
	s_nop 0
	v_mfma_f32_16x16x32_bf16 v[64:67], v[128:131], v[188:191], v[64:67]
	s_setprio 0
	s_barrier
	ds_read_b128 v[160:163], v219 offset:49152
	ds_read_b128 v[164:167], v219 offset:50176
	ds_read_b128 v[168:171], v219 offset:51200
	ds_read_b128 v[172:175], v219 offset:52224
	ds_read_b128 v[176:179], v219 offset:53248
	ds_read_b128 v[180:183], v219 offset:54272
	ds_read_b128 v[184:187], v219 offset:55296
	ds_read_b128 v[188:191], v219 offset:56320
	s_mov_b32 m0, s73
	s_mov_b32 s14, s10
	s_mov_b32 s15, s11
	buffer_load_dwordx4 v202, s[12:15], s5 offen lds
	s_add_i32 s5, s93, 0x80180
	s_mov_b32 m0, s74
	s_nop 0
	buffer_load_dwordx4 v202, s[12:15], s5 offen lds
	s_add_i32 s5, s93, 0x8180
	s_mov_b32 m0, s77
	s_nop 0
	buffer_load_dwordx4 v202, s[12:15], s5 offen lds
	s_add_i32 s5, s93, 0x88180
	s_mov_b32 m0, s78
	s_nop 0
	buffer_load_dwordx4 v202, s[12:15], s5 offen lds
	s_mov_b32 m0, s75
	s_nop 0
	buffer_load_dwordx4 v196, s[8:11], s4 offen lds
	s_add_i32 s4, s92, 0x10180
	s_mov_b32 m0, s76
	s_nop 0
	buffer_load_dwordx4 v196, s[8:11], s4 offen lds
	s_waitcnt vmcnt(8)
	s_waitcnt lgkmcnt(6)
	s_barrier
	s_setprio 1
	s_waitcnt lgkmcnt(7)
	v_mfma_f32_16x16x32_bf16 v[60:63], v[156:159], v[160:163], v[60:63]
	s_waitcnt lgkmcnt(6)
	v_mfma_f32_16x16x32_bf16 v[60:63], v[152:155], v[164:167], v[60:63]
	v_mfma_f32_16x16x32_bf16 v[56:59], v[148:151], v[160:163], v[56:59]
	s_nop 0
	v_mfma_f32_16x16x32_bf16 v[56:59], v[144:147], v[164:167], v[56:59]
	s_waitcnt lgkmcnt(5)
	v_mfma_f32_16x16x32_bf16 v[52:55], v[156:159], v[168:171], v[52:55]
	s_waitcnt lgkmcnt(4)
	v_mfma_f32_16x16x32_bf16 v[52:55], v[152:155], v[172:175], v[52:55]
	v_mfma_f32_16x16x32_bf16 v[48:51], v[148:151], v[168:171], v[48:51]
	s_nop 0
	v_mfma_f32_16x16x32_bf16 v[48:51], v[144:147], v[172:175], v[48:51]
	s_waitcnt lgkmcnt(3)
	v_mfma_f32_16x16x32_bf16 v[44:47], v[156:159], v[176:179], v[44:47]
	s_waitcnt lgkmcnt(2)
	v_mfma_f32_16x16x32_bf16 v[44:47], v[152:155], v[180:183], v[44:47]
	v_mfma_f32_16x16x32_bf16 v[40:43], v[148:151], v[176:179], v[40:43]
	s_nop 0
	v_mfma_f32_16x16x32_bf16 v[40:43], v[144:147], v[180:183], v[40:43]
	s_waitcnt lgkmcnt(1)
	v_mfma_f32_16x16x32_bf16 v[36:39], v[156:159], v[184:187], v[36:39]
	s_waitcnt lgkmcnt(0)
	v_mfma_f32_16x16x32_bf16 v[36:39], v[152:155], v[188:191], v[36:39]
	v_mfma_f32_16x16x32_bf16 v[32:35], v[148:151], v[184:187], v[32:35]
	s_nop 0
	v_mfma_f32_16x16x32_bf16 v[32:35], v[144:147], v[188:191], v[32:35]
	s_setprio 0
	s_setprio 1
	v_mfma_f32_16x16x32_bf16 v[28:31], v[140:143], v[160:163], v[28:31]
	s_nop 0
	v_mfma_f32_16x16x32_bf16 v[28:31], v[136:139], v[164:167], v[28:31]
	v_mfma_f32_16x16x32_bf16 v[24:27], v[132:135], v[160:163], v[24:27]
	s_nop 0
	v_mfma_f32_16x16x32_bf16 v[24:27], v[128:131], v[164:167], v[24:27]
	v_mfma_f32_16x16x32_bf16 v[20:23], v[140:143], v[168:171], v[20:23]
	s_nop 0
	v_mfma_f32_16x16x32_bf16 v[20:23], v[136:139], v[172:175], v[20:23]
	v_mfma_f32_16x16x32_bf16 v[16:19], v[132:135], v[168:171], v[16:19]
	s_nop 0
	v_mfma_f32_16x16x32_bf16 v[16:19], v[128:131], v[172:175], v[16:19]
	v_mfma_f32_16x16x32_bf16 v[12:15], v[140:143], v[176:179], v[12:15]
	s_nop 0
	v_mfma_f32_16x16x32_bf16 v[12:15], v[136:139], v[180:183], v[12:15]
	v_mfma_f32_16x16x32_bf16 v[8:11], v[132:135], v[176:179], v[8:11]
	s_nop 0
	v_mfma_f32_16x16x32_bf16 v[8:11], v[128:131], v[180:183], v[8:11]
	v_mfma_f32_16x16x32_bf16 v[4:7], v[140:143], v[184:187], v[4:7]
	s_nop 0
	v_mfma_f32_16x16x32_bf16 v[4:7], v[136:139], v[188:191], v[4:7]
	v_mfma_f32_16x16x32_bf16 v[0:3], v[132:135], v[184:187], v[0:3]
	s_nop 0
	v_mfma_f32_16x16x32_bf16 v[0:3], v[128:131], v[188:191], v[0:3]
	s_setprio 0
	s_barrier
	s_add_i32 s4, s92, 0x30180
	s_add_i32 s5, s93, 0x200
	s_mov_b32 s33, 0
.LBB0_220:
	ds_read_b128 v[128:131], v203
	ds_read_b128 v[132:135], v204
	ds_read_b128 v[136:139], v205
	ds_read_b128 v[140:143], v206
	ds_read_b128 v[144:147], v207
	ds_read_b128 v[148:151], v208
	ds_read_b128 v[152:155], v209
	ds_read_b128 v[156:159], v210
	ds_read_b128 v[160:163], v219
	ds_read_b128 v[164:167], v219 offset:1024
	ds_read_b128 v[168:171], v219 offset:2048
	ds_read_b128 v[172:175], v219 offset:3072
	ds_read_b128 v[176:179], v219 offset:4096
	ds_read_b128 v[180:183], v219 offset:5120
	ds_read_b128 v[184:187], v219 offset:6144
	ds_read_b128 v[188:191], v219 offset:7168
	s_add_i32 s66, s4, 0xfffd0080
	s_cmp_eq_u32 s33, 4
	s_cselect_b32 s66, s90, s66
	s_cselect_b32 s92, s91, s5
	s_add_i32 s67, s66, 0x80
	s_mov_b32 m0, s79
	s_add_i32 s93, s4, 0xffff0000
	buffer_load_dwordx4 v196, s[8:11], s93 offen lds
	s_mov_b32 m0, s81
	s_nop 0
	buffer_load_dwordx4 v196, s[8:11], s4 offen lds
	s_waitcnt vmcnt(8)
	s_waitcnt lgkmcnt(8)
	s_barrier
	s_setprio 1
	s_waitcnt lgkmcnt(7)
	v_mfma_f32_16x16x32_bf16 v[124:127], v[128:131], v[160:163], v[124:127]
	s_waitcnt lgkmcnt(6)
	v_mfma_f32_16x16x32_bf16 v[124:127], v[132:135], v[164:167], v[124:127]
	v_mfma_f32_16x16x32_bf16 v[120:123], v[136:139], v[160:163], v[120:123]
	s_nop 0
	v_mfma_f32_16x16x32_bf16 v[120:123], v[140:143], v[164:167], v[120:123]
	s_waitcnt lgkmcnt(5)
	v_mfma_f32_16x16x32_bf16 v[116:119], v[128:131], v[168:171], v[116:119]
	s_waitcnt lgkmcnt(4)
	v_mfma_f32_16x16x32_bf16 v[116:119], v[132:135], v[172:175], v[116:119]
	v_mfma_f32_16x16x32_bf16 v[112:115], v[136:139], v[168:171], v[112:115]
	s_nop 0
	v_mfma_f32_16x16x32_bf16 v[112:115], v[140:143], v[172:175], v[112:115]
	s_waitcnt lgkmcnt(3)
	v_mfma_f32_16x16x32_bf16 v[108:111], v[128:131], v[176:179], v[108:111]
	s_waitcnt lgkmcnt(2)
	v_mfma_f32_16x16x32_bf16 v[108:111], v[132:135], v[180:183], v[108:111]
	v_mfma_f32_16x16x32_bf16 v[104:107], v[136:139], v[176:179], v[104:107]
	s_nop 0
	v_mfma_f32_16x16x32_bf16 v[104:107], v[140:143], v[180:183], v[104:107]
	s_waitcnt lgkmcnt(1)
	v_mfma_f32_16x16x32_bf16 v[100:103], v[128:131], v[184:187], v[100:103]
	s_waitcnt lgkmcnt(0)
	v_mfma_f32_16x16x32_bf16 v[100:103], v[132:135], v[188:191], v[100:103]
	v_mfma_f32_16x16x32_bf16 v[96:99], v[136:139], v[184:187], v[96:99]
	s_nop 0
	v_mfma_f32_16x16x32_bf16 v[96:99], v[140:143], v[188:191], v[96:99]
	s_setprio 0
	s_setprio 1
	v_mfma_f32_16x16x32_bf16 v[92:95], v[144:147], v[160:163], v[92:95]
	s_nop 0
	v_mfma_f32_16x16x32_bf16 v[92:95], v[148:151], v[164:167], v[92:95]
	v_mfma_f32_16x16x32_bf16 v[88:91], v[152:155], v[160:163], v[88:91]
	s_nop 0
	v_mfma_f32_16x16x32_bf16 v[88:91], v[156:159], v[164:167], v[88:91]
	v_mfma_f32_16x16x32_bf16 v[84:87], v[144:147], v[168:171], v[84:87]
	s_nop 0
	v_mfma_f32_16x16x32_bf16 v[84:87], v[148:151], v[172:175], v[84:87]
	v_mfma_f32_16x16x32_bf16 v[80:83], v[152:155], v[168:171], v[80:83]
	s_nop 0
	v_mfma_f32_16x16x32_bf16 v[80:83], v[156:159], v[172:175], v[80:83]
	v_mfma_f32_16x16x32_bf16 v[76:79], v[144:147], v[176:179], v[76:79]
	s_nop 0
	v_mfma_f32_16x16x32_bf16 v[76:79], v[148:151], v[180:183], v[76:79]
	v_mfma_f32_16x16x32_bf16 v[72:75], v[152:155], v[176:179], v[72:75]
	s_nop 0
	v_mfma_f32_16x16x32_bf16 v[72:75], v[156:159], v[180:183], v[72:75]
	v_mfma_f32_16x16x32_bf16 v[68:71], v[144:147], v[184:187], v[68:71]
	s_nop 0
	v_mfma_f32_16x16x32_bf16 v[68:71], v[148:151], v[188:191], v[68:71]
	v_mfma_f32_16x16x32_bf16 v[64:67], v[152:155], v[184:187], v[64:67]
	s_nop 0
	v_mfma_f32_16x16x32_bf16 v[64:67], v[156:159], v[188:191], v[64:67]
	s_setprio 0
	s_barrier
	ds_read_b128 v[160:163], v219 offset:16384
	ds_read_b128 v[164:167], v219 offset:17408
	ds_read_b128 v[168:171], v219 offset:18432
	ds_read_b128 v[172:175], v219 offset:19456
	ds_read_b128 v[176:179], v219 offset:20480
	ds_read_b128 v[180:183], v219 offset:21504
	ds_read_b128 v[184:187], v219 offset:22528
	ds_read_b128 v[188:191], v219 offset:23552
	s_mov_b32 m0, s62
	s_add_i32 s93, s92, 0x80000
	buffer_load_dwordx4 v202, s[12:15], s92 offen lds
	s_mov_b32 m0, s63
	s_nop 0
	buffer_load_dwordx4 v202, s[12:15], s93 offen lds
	s_add_i32 s93, s92, 0x8000
	s_mov_b32 m0, s64
	s_nop 0
	buffer_load_dwordx4 v202, s[12:15], s93 offen lds
	s_add_i32 s93, s92, 0x88000
	s_mov_b32 m0, s65
	s_nop 0
	buffer_load_dwordx4 v202, s[12:15], s93 offen lds
	s_mov_b32 m0, s45
	s_add_i32 s93, s66, 0x10000
	buffer_load_dwordx4 v196, s[8:11], s66 offen lds
	s_mov_b32 m0, s68
	s_nop 0
	buffer_load_dwordx4 v196, s[8:11], s93 offen lds
	s_waitcnt vmcnt(8)
	s_waitcnt lgkmcnt(6)
	s_barrier
	s_setprio 1
	s_waitcnt lgkmcnt(7)
	v_mfma_f32_16x16x32_bf16 v[60:63], v[128:131], v[160:163], v[60:63]
	s_waitcnt lgkmcnt(6)
	v_mfma_f32_16x16x32_bf16 v[60:63], v[132:135], v[164:167], v[60:63]
	v_mfma_f32_16x16x32_bf16 v[56:59], v[136:139], v[160:163], v[56:59]
	s_nop 0
	v_mfma_f32_16x16x32_bf16 v[56:59], v[140:143], v[164:167], v[56:59]
	s_waitcnt lgkmcnt(5)
	v_mfma_f32_16x16x32_bf16 v[52:55], v[128:131], v[168:171], v[52:55]
	s_waitcnt lgkmcnt(4)
	v_mfma_f32_16x16x32_bf16 v[52:55], v[132:135], v[172:175], v[52:55]
	v_mfma_f32_16x16x32_bf16 v[48:51], v[136:139], v[168:171], v[48:51]
	s_nop 0
	v_mfma_f32_16x16x32_bf16 v[48:51], v[140:143], v[172:175], v[48:51]
	s_waitcnt lgkmcnt(3)
	v_mfma_f32_16x16x32_bf16 v[44:47], v[128:131], v[176:179], v[44:47]
	s_waitcnt lgkmcnt(2)
	v_mfma_f32_16x16x32_bf16 v[44:47], v[132:135], v[180:183], v[44:47]
	v_mfma_f32_16x16x32_bf16 v[40:43], v[136:139], v[176:179], v[40:43]
	s_nop 0
	v_mfma_f32_16x16x32_bf16 v[40:43], v[140:143], v[180:183], v[40:43]
	s_waitcnt lgkmcnt(1)
	v_mfma_f32_16x16x32_bf16 v[36:39], v[128:131], v[184:187], v[36:39]
	s_waitcnt lgkmcnt(0)
	v_mfma_f32_16x16x32_bf16 v[36:39], v[132:135], v[188:191], v[36:39]
	v_mfma_f32_16x16x32_bf16 v[32:35], v[136:139], v[184:187], v[32:35]
	s_nop 0
	v_mfma_f32_16x16x32_bf16 v[32:35], v[140:143], v[188:191], v[32:35]
	s_setprio 0
	s_setprio 1
	v_mfma_f32_16x16x32_bf16 v[28:31], v[144:147], v[160:163], v[28:31]
	s_nop 0
	v_mfma_f32_16x16x32_bf16 v[28:31], v[148:151], v[164:167], v[28:31]
	v_mfma_f32_16x16x32_bf16 v[24:27], v[152:155], v[160:163], v[24:27]
	s_nop 0
	v_mfma_f32_16x16x32_bf16 v[24:27], v[156:159], v[164:167], v[24:27]
	v_mfma_f32_16x16x32_bf16 v[20:23], v[144:147], v[168:171], v[20:23]
	s_nop 0
	v_mfma_f32_16x16x32_bf16 v[20:23], v[148:151], v[172:175], v[20:23]
	v_mfma_f32_16x16x32_bf16 v[16:19], v[152:155], v[168:171], v[16:19]
	s_nop 0
	v_mfma_f32_16x16x32_bf16 v[16:19], v[156:159], v[172:175], v[16:19]
	v_mfma_f32_16x16x32_bf16 v[12:15], v[144:147], v[176:179], v[12:15]
	s_nop 0
	v_mfma_f32_16x16x32_bf16 v[12:15], v[148:151], v[180:183], v[12:15]
	v_mfma_f32_16x16x32_bf16 v[8:11], v[152:155], v[176:179], v[8:11]
	s_nop 0
	v_mfma_f32_16x16x32_bf16 v[8:11], v[156:159], v[180:183], v[8:11]
	v_mfma_f32_16x16x32_bf16 v[4:7], v[144:147], v[184:187], v[4:7]
	s_nop 0
	v_mfma_f32_16x16x32_bf16 v[4:7], v[148:151], v[188:191], v[4:7]
	v_mfma_f32_16x16x32_bf16 v[0:3], v[152:155], v[184:187], v[0:3]
	s_nop 0
	v_mfma_f32_16x16x32_bf16 v[0:3], v[156:159], v[188:191], v[0:3]
	s_setprio 0
	s_barrier
	ds_read_b128 v[140:143], v211
	ds_read_b128 v[144:147], v212
	ds_read_b128 v[148:151], v213
	ds_read_b128 v[152:155], v214
	ds_read_b128 v[156:159], v215
	ds_read_b128 v[136:139], v216
	ds_read_b128 v[132:135], v217
	ds_read_b128 v[128:131], v218
	ds_read_b128 v[160:163], v219 offset:32768
	ds_read_b128 v[164:167], v219 offset:33792
	ds_read_b128 v[168:171], v219 offset:34816
	ds_read_b128 v[172:175], v219 offset:35840
	ds_read_b128 v[176:179], v219 offset:36864
	ds_read_b128 v[180:183], v219 offset:37888
	ds_read_b128 v[184:187], v219 offset:38912
	ds_read_b128 v[188:191], v219 offset:39936
	s_mov_b32 m0, s69
	s_add_i32 s93, s66, 0x20000
	buffer_load_dwordx4 v196, s[8:11], s93 offen lds
	s_add_i32 s93, s66, 0x30000
	s_mov_b32 m0, s70
	s_nop 0
	buffer_load_dwordx4 v196, s[8:11], s93 offen lds
	s_waitcnt vmcnt(8)
	s_waitcnt lgkmcnt(8)
	s_barrier
	s_setprio 1
	s_waitcnt lgkmcnt(7)
	v_mfma_f32_16x16x32_bf16 v[124:127], v[140:143], v[160:163], v[124:127]
	s_waitcnt lgkmcnt(6)
	v_mfma_f32_16x16x32_bf16 v[124:127], v[144:147], v[164:167], v[124:127]
	v_mfma_f32_16x16x32_bf16 v[120:123], v[148:151], v[160:163], v[120:123]
	s_nop 0
	v_mfma_f32_16x16x32_bf16 v[120:123], v[152:155], v[164:167], v[120:123]
	s_waitcnt lgkmcnt(5)
	v_mfma_f32_16x16x32_bf16 v[116:119], v[140:143], v[168:171], v[116:119]
	s_waitcnt lgkmcnt(4)
	v_mfma_f32_16x16x32_bf16 v[116:119], v[144:147], v[172:175], v[116:119]
	v_mfma_f32_16x16x32_bf16 v[112:115], v[148:151], v[168:171], v[112:115]
	s_nop 0
	v_mfma_f32_16x16x32_bf16 v[112:115], v[152:155], v[172:175], v[112:115]
	s_waitcnt lgkmcnt(3)
	v_mfma_f32_16x16x32_bf16 v[108:111], v[140:143], v[176:179], v[108:111]
	s_waitcnt lgkmcnt(2)
	v_mfma_f32_16x16x32_bf16 v[108:111], v[144:147], v[180:183], v[108:111]
	v_mfma_f32_16x16x32_bf16 v[104:107], v[148:151], v[176:179], v[104:107]
	s_nop 0
	v_mfma_f32_16x16x32_bf16 v[104:107], v[152:155], v[180:183], v[104:107]
	s_waitcnt lgkmcnt(1)
	v_mfma_f32_16x16x32_bf16 v[100:103], v[140:143], v[184:187], v[100:103]
	s_waitcnt lgkmcnt(0)
	v_mfma_f32_16x16x32_bf16 v[100:103], v[144:147], v[188:191], v[100:103]
	v_mfma_f32_16x16x32_bf16 v[96:99], v[148:151], v[184:187], v[96:99]
	s_nop 0
	v_mfma_f32_16x16x32_bf16 v[96:99], v[152:155], v[188:191], v[96:99]
	s_setprio 0
	s_setprio 1
	v_mfma_f32_16x16x32_bf16 v[92:95], v[156:159], v[160:163], v[92:95]
	s_nop 0
	v_mfma_f32_16x16x32_bf16 v[92:95], v[136:139], v[164:167], v[92:95]
	v_mfma_f32_16x16x32_bf16 v[88:91], v[132:135], v[160:163], v[88:91]
	s_nop 0
	v_mfma_f32_16x16x32_bf16 v[88:91], v[128:131], v[164:167], v[88:91]
	v_mfma_f32_16x16x32_bf16 v[84:87], v[156:159], v[168:171], v[84:87]
	s_nop 0
	v_mfma_f32_16x16x32_bf16 v[84:87], v[136:139], v[172:175], v[84:87]
	v_mfma_f32_16x16x32_bf16 v[80:83], v[132:135], v[168:171], v[80:83]
	s_nop 0
	v_mfma_f32_16x16x32_bf16 v[80:83], v[128:131], v[172:175], v[80:83]
	v_mfma_f32_16x16x32_bf16 v[76:79], v[156:159], v[176:179], v[76:79]
	s_nop 0
	v_mfma_f32_16x16x32_bf16 v[76:79], v[136:139], v[180:183], v[76:79]
	v_mfma_f32_16x16x32_bf16 v[72:75], v[132:135], v[176:179], v[72:75]
	s_nop 0
	v_mfma_f32_16x16x32_bf16 v[72:75], v[128:131], v[180:183], v[72:75]
	v_mfma_f32_16x16x32_bf16 v[68:71], v[156:159], v[184:187], v[68:71]
	s_nop 0
	v_mfma_f32_16x16x32_bf16 v[68:71], v[136:139], v[188:191], v[68:71]
	v_mfma_f32_16x16x32_bf16 v[64:67], v[132:135], v[184:187], v[64:67]
	s_nop 0
	v_mfma_f32_16x16x32_bf16 v[64:67], v[128:131], v[188:191], v[64:67]
	s_setprio 0
	s_barrier
	ds_read_b128 v[160:163], v219 offset:49152
	ds_read_b128 v[164:167], v219 offset:50176
	ds_read_b128 v[168:171], v219 offset:51200
	ds_read_b128 v[172:175], v219 offset:52224
	ds_read_b128 v[176:179], v219 offset:53248
	ds_read_b128 v[180:183], v219 offset:54272
	ds_read_b128 v[184:187], v219 offset:55296
	ds_read_b128 v[188:191], v219 offset:56320
	s_mov_b32 m0, s73
	s_add_i32 s93, s92, 0x80
	buffer_load_dwordx4 v202, s[12:15], s93 offen lds
	s_add_i32 s93, s92, 0x80080
	s_mov_b32 m0, s74
	s_add_i32 s66, s66, 0x10080
	buffer_load_dwordx4 v202, s[12:15], s93 offen lds
	s_add_i32 s93, s92, 0x8080
	s_mov_b32 m0, s77
	s_add_i32 s92, s92, 0x88080
	buffer_load_dwordx4 v202, s[12:15], s93 offen lds
	s_mov_b32 m0, s78
	s_nop 0
	buffer_load_dwordx4 v202, s[12:15], s92 offen lds
	s_mov_b32 m0, s75
	s_nop 0
	buffer_load_dwordx4 v196, s[8:11], s67 offen lds
	s_mov_b32 m0, s76
	s_nop 0
	buffer_load_dwordx4 v196, s[8:11], s66 offen lds
	s_waitcnt vmcnt(8)
	s_waitcnt lgkmcnt(6)
	s_barrier
	s_setprio 1
	s_waitcnt lgkmcnt(7)
	v_mfma_f32_16x16x32_bf16 v[60:63], v[140:143], v[160:163], v[60:63]
	s_waitcnt lgkmcnt(6)
	v_mfma_f32_16x16x32_bf16 v[60:63], v[144:147], v[164:167], v[60:63]
	v_mfma_f32_16x16x32_bf16 v[56:59], v[148:151], v[160:163], v[56:59]
	s_nop 0
	v_mfma_f32_16x16x32_bf16 v[56:59], v[152:155], v[164:167], v[56:59]
	s_waitcnt lgkmcnt(5)
	v_mfma_f32_16x16x32_bf16 v[52:55], v[140:143], v[168:171], v[52:55]
	s_waitcnt lgkmcnt(4)
	v_mfma_f32_16x16x32_bf16 v[52:55], v[144:147], v[172:175], v[52:55]
	v_mfma_f32_16x16x32_bf16 v[48:51], v[148:151], v[168:171], v[48:51]
	s_nop 0
	v_mfma_f32_16x16x32_bf16 v[48:51], v[152:155], v[172:175], v[48:51]
	s_waitcnt lgkmcnt(3)
	v_mfma_f32_16x16x32_bf16 v[44:47], v[140:143], v[176:179], v[44:47]
	s_waitcnt lgkmcnt(2)
	v_mfma_f32_16x16x32_bf16 v[44:47], v[144:147], v[180:183], v[44:47]
	v_mfma_f32_16x16x32_bf16 v[40:43], v[148:151], v[176:179], v[40:43]
	s_nop 0
	v_mfma_f32_16x16x32_bf16 v[40:43], v[152:155], v[180:183], v[40:43]
	s_waitcnt lgkmcnt(1)
	v_mfma_f32_16x16x32_bf16 v[36:39], v[140:143], v[184:187], v[36:39]
	s_waitcnt lgkmcnt(0)
	v_mfma_f32_16x16x32_bf16 v[36:39], v[144:147], v[188:191], v[36:39]
	v_mfma_f32_16x16x32_bf16 v[32:35], v[148:151], v[184:187], v[32:35]
	s_nop 0
	v_mfma_f32_16x16x32_bf16 v[32:35], v[152:155], v[188:191], v[32:35]
	s_setprio 0
	s_setprio 1
	v_mfma_f32_16x16x32_bf16 v[28:31], v[156:159], v[160:163], v[28:31]
	s_nop 0
	v_mfma_f32_16x16x32_bf16 v[28:31], v[136:139], v[164:167], v[28:31]
	v_mfma_f32_16x16x32_bf16 v[24:27], v[132:135], v[160:163], v[24:27]
	s_nop 0
	v_mfma_f32_16x16x32_bf16 v[24:27], v[128:131], v[164:167], v[24:27]
	v_mfma_f32_16x16x32_bf16 v[20:23], v[156:159], v[168:171], v[20:23]
	s_nop 0
	v_mfma_f32_16x16x32_bf16 v[20:23], v[136:139], v[172:175], v[20:23]
	v_mfma_f32_16x16x32_bf16 v[16:19], v[132:135], v[168:171], v[16:19]
	s_nop 0
	v_mfma_f32_16x16x32_bf16 v[16:19], v[128:131], v[172:175], v[16:19]
	v_mfma_f32_16x16x32_bf16 v[12:15], v[156:159], v[176:179], v[12:15]
	s_nop 0
	v_mfma_f32_16x16x32_bf16 v[12:15], v[136:139], v[180:183], v[12:15]
	v_mfma_f32_16x16x32_bf16 v[8:11], v[132:135], v[176:179], v[8:11]
	s_nop 0
	v_mfma_f32_16x16x32_bf16 v[8:11], v[128:131], v[180:183], v[8:11]
	v_mfma_f32_16x16x32_bf16 v[4:7], v[156:159], v[184:187], v[4:7]
	s_nop 0
	v_mfma_f32_16x16x32_bf16 v[4:7], v[136:139], v[188:191], v[4:7]
	v_mfma_f32_16x16x32_bf16 v[0:3], v[132:135], v[184:187], v[0:3]
	s_nop 0
	v_mfma_f32_16x16x32_bf16 v[0:3], v[128:131], v[188:191], v[0:3]
	s_setprio 0
	s_barrier
	s_add_i32 s33, s33, 2
	s_addk_i32 s4, 0x100
	s_addk_i32 s5, 0x100
	s_cmp_gt_u32 s33, 5
	s_cbranch_scc0 .LBB0_220
	s_and_b64 vcc, exec, s[16:17]
	s_cbranch_vccz .LBB0_223
	s_barrier

.LBB0_253:
	s_waitcnt lgkmcnt(0)
	s_add_i32 s33, s91, 0x180
	s_add_i32 s42, s90, 0x180
	s_barrier
	s_setprio 1
	s_waitcnt lgkmcnt(7)
	v_mfma_f32_16x16x32_bf16 v[60:63], v[156:159], v[188:191], 0
	s_waitcnt lgkmcnt(6)
	v_mfma_f32_16x16x32_bf16 v[60:63], v[152:155], v[184:187], v[60:63]
	v_mfma_f32_16x16x32_bf16 v[56:59], v[148:151], v[188:191], 0
	s_nop 0
	v_mfma_f32_16x16x32_bf16 v[56:59], v[144:147], v[184:187], v[56:59]
	s_waitcnt lgkmcnt(5)
	v_mfma_f32_16x16x32_bf16 v[52:55], v[156:159], v[180:183], 0
	s_waitcnt lgkmcnt(4)
	v_mfma_f32_16x16x32_bf16 v[52:55], v[152:155], v[176:179], v[52:55]
	v_mfma_f32_16x16x32_bf16 v[48:51], v[148:151], v[180:183], 0
	s_nop 0
	v_mfma_f32_16x16x32_bf16 v[48:51], v[144:147], v[176:179], v[48:51]
	s_waitcnt lgkmcnt(3)
	v_mfma_f32_16x16x32_bf16 v[44:47], v[156:159], v[172:175], 0
	s_waitcnt lgkmcnt(2)
	v_mfma_f32_16x16x32_bf16 v[44:47], v[152:155], v[168:171], v[44:47]
	v_mfma_f32_16x16x32_bf16 v[40:43], v[148:151], v[172:175], 0
	s_nop 0
	v_mfma_f32_16x16x32_bf16 v[40:43], v[144:147], v[168:171], v[40:43]
	s_waitcnt lgkmcnt(1)
	v_mfma_f32_16x16x32_bf16 v[36:39], v[156:159], v[164:167], 0
	s_waitcnt lgkmcnt(0)
	v_mfma_f32_16x16x32_bf16 v[36:39], v[152:155], v[160:163], v[36:39]
	v_mfma_f32_16x16x32_bf16 v[32:35], v[148:151], v[164:167], 0
	s_nop 0
	v_mfma_f32_16x16x32_bf16 v[32:35], v[144:147], v[160:163], v[32:35]
	s_setprio 0
	s_setprio 1
	v_mfma_f32_16x16x32_bf16 v[28:31], v[140:143], v[188:191], 0
	s_nop 0
	v_mfma_f32_16x16x32_bf16 v[28:31], v[136:139], v[184:187], v[28:31]
	v_mfma_f32_16x16x32_bf16 v[24:27], v[132:135], v[188:191], 0
	s_nop 0
	v_mfma_f32_16x16x32_bf16 v[24:27], v[128:131], v[184:187], v[24:27]
	v_mfma_f32_16x16x32_bf16 v[20:23], v[140:143], v[180:183], 0
	s_nop 0
	v_mfma_f32_16x16x32_bf16 v[20:23], v[136:139], v[176:179], v[20:23]
	v_mfma_f32_16x16x32_bf16 v[16:19], v[132:135], v[180:183], 0
	s_nop 0
	v_mfma_f32_16x16x32_bf16 v[16:19], v[128:131], v[176:179], v[16:19]
	v_mfma_f32_16x16x32_bf16 v[12:15], v[140:143], v[172:175], 0
	s_nop 0
	v_mfma_f32_16x16x32_bf16 v[12:15], v[136:139], v[168:171], v[12:15]
	v_mfma_f32_16x16x32_bf16 v[8:11], v[132:135], v[172:175], 0
	s_nop 0
	v_mfma_f32_16x16x32_bf16 v[8:11], v[128:131], v[168:171], v[8:11]
	v_mfma_f32_16x16x32_bf16 v[4:7], v[140:143], v[164:167], 0
	s_nop 0
	v_mfma_f32_16x16x32_bf16 v[4:7], v[136:139], v[160:163], v[4:7]
	v_mfma_f32_16x16x32_bf16 v[0:3], v[132:135], v[164:167], 0
	s_nop 0
	v_mfma_f32_16x16x32_bf16 v[0:3], v[128:131], v[160:163], v[0:3]
	s_setprio 0
	s_barrier
	ds_read_b128 v[156:159], v203
	ds_read_b128 v[152:155], v204
	ds_read_b128 v[148:151], v205
	ds_read_b128 v[144:147], v206
	ds_read_b128 v[140:143], v207
	ds_read_b128 v[136:139], v208
	ds_read_b128 v[132:135], v209
	ds_read_b128 v[128:131], v210
	ds_read_b128 v[160:163], v197 offset:32768
	ds_read_b128 v[164:167], v197 offset:33792
	ds_read_b128 v[168:171], v197 offset:34816
	ds_read_b128 v[172:175], v197 offset:35840
	ds_read_b128 v[176:179], v197 offset:36864
	ds_read_b128 v[180:183], v197 offset:37888
	ds_read_b128 v[184:187], v197 offset:38912
	ds_read_b128 v[188:191], v197 offset:39936
	s_mov_b32 m0, s69
	s_add_i32 s10, s91, 0x20100
	buffer_load_dwordx4 v196, s[4:7], s10 offen lds
	s_add_i32 s10, s91, 0x30100
	s_mov_b32 m0, s70
	s_nop 0
	buffer_load_dwordx4 v196, s[4:7], s10 offen lds
	s_waitcnt vmcnt(8)
	s_waitcnt lgkmcnt(8)
	s_barrier
	s_setprio 1
	s_waitcnt lgkmcnt(7)
	v_mfma_f32_16x16x32_bf16 v[124:127], v[156:159], v[160:163], v[124:127]
	s_waitcnt lgkmcnt(6)
	v_mfma_f32_16x16x32_bf16 v[124:127], v[152:155], v[164:167], v[124:127]
	v_mfma_f32_16x16x32_bf16 v[120:123], v[148:151], v[160:163], v[120:123]
	s_nop 0
	v_mfma_f32_16x16x32_bf16 v[120:123], v[144:147], v[164:167], v[120:123]
	s_waitcnt lgkmcnt(5)
	v_mfma_f32_16x16x32_bf16 v[116:119], v[156:159], v[168:171], v[116:119]
	s_waitcnt lgkmcnt(4)
	v_mfma_f32_16x16x32_bf16 v[116:119], v[152:155], v[172:175], v[116:119]
	v_mfma_f32_16x16x32_bf16 v[112:115], v[148:151], v[168:171], v[112:115]
	s_nop 0
	v_mfma_f32_16x16x32_bf16 v[112:115], v[144:147], v[172:175], v[112:115]
	s_waitcnt lgkmcnt(3)
	v_mfma_f32_16x16x32_bf16 v[108:111], v[156:159], v[176:179], v[108:111]
	s_waitcnt lgkmcnt(2)
	v_mfma_f32_16x16x32_bf16 v[108:111], v[152:155], v[180:183], v[108:111]
	v_mfma_f32_16x16x32_bf16 v[104:107], v[148:151], v[176:179], v[104:107]
	s_nop 0
	v_mfma_f32_16x16x32_bf16 v[104:107], v[144:147], v[180:183], v[104:107]
	s_waitcnt lgkmcnt(1)
	v_mfma_f32_16x16x32_bf16 v[100:103], v[156:159], v[184:187], v[100:103]
	s_waitcnt lgkmcnt(0)
	v_mfma_f32_16x16x32_bf16 v[100:103], v[152:155], v[188:191], v[100:103]
	v_mfma_f32_16x16x32_bf16 v[96:99], v[148:151], v[184:187], v[96:99]
	s_nop 0
	v_mfma_f32_16x16x32_bf16 v[96:99], v[144:147], v[188:191], v[96:99]
	s_setprio 0
	s_setprio 1
	v_mfma_f32_16x16x32_bf16 v[92:95], v[140:143], v[160:163], v[92:95]
	s_nop 0
	v_mfma_f32_16x16x32_bf16 v[92:95], v[136:139], v[164:167], v[92:95]
	v_mfma_f32_16x16x32_bf16 v[88:91], v[132:135], v[160:163], v[88:91]
	s_nop 0
	v_mfma_f32_16x16x32_bf16 v[88:91], v[128:131], v[164:167], v[88:91]
	v_mfma_f32_16x16x32_bf16 v[84:87], v[140:143], v[168:171], v[84:87]
	s_nop 0
	v_mfma_f32_16x16x32_bf16 v[84:87], v[136:139], v[172:175], v[84:87]
	v_mfma_f32_16x16x32_bf16 v[80:83], v[132:135], v[168:171], v[80:83]
	s_nop 0
	v_mfma_f32_16x16x32_bf16 v[80:83], v[128:131], v[172:175], v[80:83]
	v_mfma_f32_16x16x32_bf16 v[76:79], v[140:143], v[176:179], v[76:79]
	s_nop 0
	v_mfma_f32_16x16x32_bf16 v[76:79], v[136:139], v[180:183], v[76:79]
	v_mfma_f32_16x16x32_bf16 v[72:75], v[132:135], v[176:179], v[72:75]
	s_nop 0
	v_mfma_f32_16x16x32_bf16 v[72:75], v[128:131], v[180:183], v[72:75]
	v_mfma_f32_16x16x32_bf16 v[68:71], v[140:143], v[184:187], v[68:71]
	s_nop 0
	v_mfma_f32_16x16x32_bf16 v[68:71], v[136:139], v[188:191], v[68:71]
	v_mfma_f32_16x16x32_bf16 v[64:67], v[132:135], v[184:187], v[64:67]
	s_nop 0
	v_mfma_f32_16x16x32_bf16 v[64:67], v[128:131], v[188:191], v[64:67]
	s_setprio 0
	s_barrier
	ds_read_b128 v[160:163], v197 offset:49152
	ds_read_b128 v[164:167], v197 offset:50176
	ds_read_b128 v[168:171], v197 offset:51200
	ds_read_b128 v[172:175], v197 offset:52224
	ds_read_b128 v[176:179], v197 offset:53248
	ds_read_b128 v[180:183], v197 offset:54272
	ds_read_b128 v[184:187], v197 offset:55296
	ds_read_b128 v[188:191], v197 offset:56320
	s_mov_b32 m0, s72
	s_mov_b32 s10, s6
	s_mov_b32 s11, s7
	buffer_load_dwordx4 v192, s[8:11], s42 offen lds
	s_add_i32 s42, s90, 0x20180
	s_mov_b32 m0, s73
	s_nop 0
	buffer_load_dwordx4 v192, s[8:11], s42 offen lds
	s_add_i32 s42, s90, 0x2180
	s_mov_b32 m0, s76
	s_nop 0
	buffer_load_dwordx4 v192, s[8:11], s42 offen lds
	s_add_i32 s42, s90, 0x22180
	s_mov_b32 m0, s77
	s_nop 0
	buffer_load_dwordx4 v192, s[8:11], s42 offen lds
	s_mov_b32 m0, s74
	s_nop 0
	buffer_load_dwordx4 v196, s[4:7], s33 offen lds
	s_add_i32 s33, s91, 0x10180
	s_mov_b32 m0, s75
	s_nop 0
	buffer_load_dwordx4 v196, s[4:7], s33 offen lds
	s_waitcnt vmcnt(8)
	s_waitcnt lgkmcnt(6)
	s_barrier
	s_setprio 1
	s_waitcnt lgkmcnt(7)
	v_mfma_f32_16x16x32_bf16 v[60:63], v[156:159], v[160:163], v[60:63]
	s_waitcnt lgkmcnt(6)
	v_mfma_f32_16x16x32_bf16 v[60:63], v[152:155], v[164:167], v[60:63]
	v_mfma_f32_16x16x32_bf16 v[56:59], v[148:151], v[160:163], v[56:59]
	s_nop 0
	v_mfma_f32_16x16x32_bf16 v[56:59], v[144:147], v[164:167], v[56:59]
	s_waitcnt lgkmcnt(5)
	v_mfma_f32_16x16x32_bf16 v[52:55], v[156:159], v[168:171], v[52:55]
	s_waitcnt lgkmcnt(4)
	v_mfma_f32_16x16x32_bf16 v[52:55], v[152:155], v[172:175], v[52:55]
	v_mfma_f32_16x16x32_bf16 v[48:51], v[148:151], v[168:171], v[48:51]
	s_nop 0
	v_mfma_f32_16x16x32_bf16 v[48:51], v[144:147], v[172:175], v[48:51]
	s_waitcnt lgkmcnt(3)
	v_mfma_f32_16x16x32_bf16 v[44:47], v[156:159], v[176:179], v[44:47]
	s_waitcnt lgkmcnt(2)
	v_mfma_f32_16x16x32_bf16 v[44:47], v[152:155], v[180:183], v[44:47]
	v_mfma_f32_16x16x32_bf16 v[40:43], v[148:151], v[176:179], v[40:43]
	s_nop 0
	v_mfma_f32_16x16x32_bf16 v[40:43], v[144:147], v[180:183], v[40:43]
	s_waitcnt lgkmcnt(1)
	v_mfma_f32_16x16x32_bf16 v[36:39], v[156:159], v[184:187], v[36:39]
	s_waitcnt lgkmcnt(0)
	v_mfma_f32_16x16x32_bf16 v[36:39], v[152:155], v[188:191], v[36:39]
	v_mfma_f32_16x16x32_bf16 v[32:35], v[148:151], v[184:187], v[32:35]
	s_nop 0
	v_mfma_f32_16x16x32_bf16 v[32:35], v[144:147], v[188:191], v[32:35]
	s_setprio 0
	s_setprio 1
	v_mfma_f32_16x16x32_bf16 v[28:31], v[140:143], v[160:163], v[28:31]
	s_nop 0
	v_mfma_f32_16x16x32_bf16 v[28:31], v[136:139], v[164:167], v[28:31]
	v_mfma_f32_16x16x32_bf16 v[24:27], v[132:135], v[160:163], v[24:27]
	s_nop 0
	v_mfma_f32_16x16x32_bf16 v[24:27], v[128:131], v[164:167], v[24:27]
	v_mfma_f32_16x16x32_bf16 v[20:23], v[140:143], v[168:171], v[20:23]
	s_nop 0
	v_mfma_f32_16x16x32_bf16 v[20:23], v[136:139], v[172:175], v[20:23]
	v_mfma_f32_16x16x32_bf16 v[16:19], v[132:135], v[168:171], v[16:19]
	s_nop 0
	v_mfma_f32_16x16x32_bf16 v[16:19], v[128:131], v[172:175], v[16:19]
	v_mfma_f32_16x16x32_bf16 v[12:15], v[140:143], v[176:179], v[12:15]
	s_nop 0
	v_mfma_f32_16x16x32_bf16 v[12:15], v[136:139], v[180:183], v[12:15]
	v_mfma_f32_16x16x32_bf16 v[8:11], v[132:135], v[176:179], v[8:11]
	s_nop 0
	v_mfma_f32_16x16x32_bf16 v[8:11], v[128:131], v[180:183], v[8:11]
	v_mfma_f32_16x16x32_bf16 v[4:7], v[140:143], v[184:187], v[4:7]
	s_nop 0
	v_mfma_f32_16x16x32_bf16 v[4:7], v[136:139], v[188:191], v[4:7]
	v_mfma_f32_16x16x32_bf16 v[0:3], v[132:135], v[184:187], v[0:3]
	s_nop 0
	v_mfma_f32_16x16x32_bf16 v[0:3], v[128:131], v[188:191], v[0:3]
	s_setprio 0
	s_barrier
	s_add_i32 s33, s91, 0x30180
	s_add_i32 s42, s90, 0x200
	s_mov_b32 s43, 0
.LBB0_254:
	ds_read_b128 v[128:131], v193
	ds_read_b128 v[132:135], v194
	ds_read_b128 v[136:139], v195
	ds_read_b128 v[140:143], v198
	ds_read_b128 v[144:147], v199
	ds_read_b128 v[148:151], v200
	ds_read_b128 v[152:155], v201
	ds_read_b128 v[156:159], v202
	ds_read_b128 v[160:163], v197
	ds_read_b128 v[164:167], v197 offset:1024
	ds_read_b128 v[168:171], v197 offset:2048
	ds_read_b128 v[172:175], v197 offset:3072
	ds_read_b128 v[176:179], v197 offset:4096
	ds_read_b128 v[180:183], v197 offset:5120
	ds_read_b128 v[184:187], v197 offset:6144
	ds_read_b128 v[188:191], v197 offset:7168
	s_add_i32 s66, s33, 0xfffd0080
	s_cmp_eq_u32 s43, 4
	s_cselect_b32 s66, s88, s66
	s_cselect_b32 s90, s89, s42
	s_add_i32 s67, s66, 0x80
	s_mov_b32 m0, s78
	s_add_i32 s91, s33, 0xffff0000
	buffer_load_dwordx4 v196, s[4:7], s91 offen lds
	s_mov_b32 m0, s79
	s_nop 0
	buffer_load_dwordx4 v196, s[4:7], s33 offen lds
	s_waitcnt vmcnt(8)
	s_waitcnt lgkmcnt(8)
	s_barrier
	s_setprio 1
	s_waitcnt lgkmcnt(7)
	v_mfma_f32_16x16x32_bf16 v[124:127], v[128:131], v[160:163], v[124:127]
	s_waitcnt lgkmcnt(6)
	v_mfma_f32_16x16x32_bf16 v[124:127], v[132:135], v[164:167], v[124:127]
	v_mfma_f32_16x16x32_bf16 v[120:123], v[136:139], v[160:163], v[120:123]
	s_nop 0
	v_mfma_f32_16x16x32_bf16 v[120:123], v[140:143], v[164:167], v[120:123]
	s_waitcnt lgkmcnt(5)
	v_mfma_f32_16x16x32_bf16 v[116:119], v[128:131], v[168:171], v[116:119]
	s_waitcnt lgkmcnt(4)
	v_mfma_f32_16x16x32_bf16 v[116:119], v[132:135], v[172:175], v[116:119]
	v_mfma_f32_16x16x32_bf16 v[112:115], v[136:139], v[168:171], v[112:115]
	s_nop 0
	v_mfma_f32_16x16x32_bf16 v[112:115], v[140:143], v[172:175], v[112:115]
	s_waitcnt lgkmcnt(3)
	v_mfma_f32_16x16x32_bf16 v[108:111], v[128:131], v[176:179], v[108:111]
	s_waitcnt lgkmcnt(2)
	v_mfma_f32_16x16x32_bf16 v[108:111], v[132:135], v[180:183], v[108:111]
	v_mfma_f32_16x16x32_bf16 v[104:107], v[136:139], v[176:179], v[104:107]
	s_nop 0
	v_mfma_f32_16x16x32_bf16 v[104:107], v[140:143], v[180:183], v[104:107]
	s_waitcnt lgkmcnt(1)
	v_mfma_f32_16x16x32_bf16 v[100:103], v[128:131], v[184:187], v[100:103]
	s_waitcnt lgkmcnt(0)
	v_mfma_f32_16x16x32_bf16 v[100:103], v[132:135], v[188:191], v[100:103]
	v_mfma_f32_16x16x32_bf16 v[96:99], v[136:139], v[184:187], v[96:99]
	s_nop 0
	v_mfma_f32_16x16x32_bf16 v[96:99], v[140:143], v[188:191], v[96:99]
	s_setprio 0
	s_setprio 1
	v_mfma_f32_16x16x32_bf16 v[92:95], v[144:147], v[160:163], v[92:95]
	s_nop 0
	v_mfma_f32_16x16x32_bf16 v[92:95], v[148:151], v[164:167], v[92:95]
	v_mfma_f32_16x16x32_bf16 v[88:91], v[152:155], v[160:163], v[88:91]
	s_nop 0
	v_mfma_f32_16x16x32_bf16 v[88:91], v[156:159], v[164:167], v[88:91]
	v_mfma_f32_16x16x32_bf16 v[84:87], v[144:147], v[168:171], v[84:87]
	s_nop 0
	v_mfma_f32_16x16x32_bf16 v[84:87], v[148:151], v[172:175], v[84:87]
	v_mfma_f32_16x16x32_bf16 v[80:83], v[152:155], v[168:171], v[80:83]
	s_nop 0
	v_mfma_f32_16x16x32_bf16 v[80:83], v[156:159], v[172:175], v[80:83]
	v_mfma_f32_16x16x32_bf16 v[76:79], v[144:147], v[176:179], v[76:79]
	s_nop 0
	v_mfma_f32_16x16x32_bf16 v[76:79], v[148:151], v[180:183], v[76:79]
	v_mfma_f32_16x16x32_bf16 v[72:75], v[152:155], v[176:179], v[72:75]
	s_nop 0
	v_mfma_f32_16x16x32_bf16 v[72:75], v[156:159], v[180:183], v[72:75]
	v_mfma_f32_16x16x32_bf16 v[68:71], v[144:147], v[184:187], v[68:71]
	s_nop 0
	v_mfma_f32_16x16x32_bf16 v[68:71], v[148:151], v[188:191], v[68:71]
	v_mfma_f32_16x16x32_bf16 v[64:67], v[152:155], v[184:187], v[64:67]
	s_nop 0
	v_mfma_f32_16x16x32_bf16 v[64:67], v[156:159], v[188:191], v[64:67]
	s_setprio 0
	s_barrier
	ds_read_b128 v[160:163], v197 offset:16384
	ds_read_b128 v[164:167], v197 offset:17408
	ds_read_b128 v[168:171], v197 offset:18432
	ds_read_b128 v[172:175], v197 offset:19456
	ds_read_b128 v[176:179], v197 offset:20480
	ds_read_b128 v[180:183], v197 offset:21504
	ds_read_b128 v[184:187], v197 offset:22528
	ds_read_b128 v[188:191], v197 offset:23552
	s_mov_b32 m0, s62
	s_add_i32 s91, s90, 0x20000
	buffer_load_dwordx4 v192, s[8:11], s90 offen lds
	s_mov_b32 m0, s63
	s_nop 0
	buffer_load_dwordx4 v192, s[8:11], s91 offen lds
	s_add_i32 s91, s90, 0x2000
	s_mov_b32 m0, s64
	s_nop 0
	buffer_load_dwordx4 v192, s[8:11], s91 offen lds
	s_add_i32 s91, s90, 0x22000
	s_mov_b32 m0, s65
	s_nop 0
	buffer_load_dwordx4 v192, s[8:11], s91 offen lds
	s_mov_b32 m0, s47
	s_add_i32 s91, s66, 0x10000
	buffer_load_dwordx4 v196, s[4:7], s66 offen lds
	s_mov_b32 m0, s68
	s_nop 0
	buffer_load_dwordx4 v196, s[4:7], s91 offen lds
	s_waitcnt vmcnt(8)
	s_waitcnt lgkmcnt(6)
	s_barrier
	s_setprio 1
	s_waitcnt lgkmcnt(7)
	v_mfma_f32_16x16x32_bf16 v[60:63], v[128:131], v[160:163], v[60:63]
	s_waitcnt lgkmcnt(6)
	v_mfma_f32_16x16x32_bf16 v[60:63], v[132:135], v[164:167], v[60:63]
	v_mfma_f32_16x16x32_bf16 v[56:59], v[136:139], v[160:163], v[56:59]
	s_nop 0
	v_mfma_f32_16x16x32_bf16 v[56:59], v[140:143], v[164:167], v[56:59]
	s_waitcnt lgkmcnt(5)
	v_mfma_f32_16x16x32_bf16 v[52:55], v[128:131], v[168:171], v[52:55]
	s_waitcnt lgkmcnt(4)
	v_mfma_f32_16x16x32_bf16 v[52:55], v[132:135], v[172:175], v[52:55]
	v_mfma_f32_16x16x32_bf16 v[48:51], v[136:139], v[168:171], v[48:51]
	s_nop 0
	v_mfma_f32_16x16x32_bf16 v[48:51], v[140:143], v[172:175], v[48:51]
	s_waitcnt lgkmcnt(3)
	v_mfma_f32_16x16x32_bf16 v[44:47], v[128:131], v[176:179], v[44:47]
	s_waitcnt lgkmcnt(2)
	v_mfma_f32_16x16x32_bf16 v[44:47], v[132:135], v[180:183], v[44:47]
	v_mfma_f32_16x16x32_bf16 v[40:43], v[136:139], v[176:179], v[40:43]
	s_nop 0
	v_mfma_f32_16x16x32_bf16 v[40:43], v[140:143], v[180:183], v[40:43]
	s_waitcnt lgkmcnt(1)
	v_mfma_f32_16x16x32_bf16 v[36:39], v[128:131], v[184:187], v[36:39]
	s_waitcnt lgkmcnt(0)
	v_mfma_f32_16x16x32_bf16 v[36:39], v[132:135], v[188:191], v[36:39]
	v_mfma_f32_16x16x32_bf16 v[32:35], v[136:139], v[184:187], v[32:35]
	s_nop 0
	v_mfma_f32_16x16x32_bf16 v[32:35], v[140:143], v[188:191], v[32:35]
	s_setprio 0
	s_setprio 1
	v_mfma_f32_16x16x32_bf16 v[28:31], v[144:147], v[160:163], v[28:31]
	s_nop 0
	v_mfma_f32_16x16x32_bf16 v[28:31], v[148:151], v[164:167], v[28:31]
	v_mfma_f32_16x16x32_bf16 v[24:27], v[152:155], v[160:163], v[24:27]
	s_nop 0
	v_mfma_f32_16x16x32_bf16 v[24:27], v[156:159], v[164:167], v[24:27]
	v_mfma_f32_16x16x32_bf16 v[20:23], v[144:147], v[168:171], v[20:23]
	s_nop 0
	v_mfma_f32_16x16x32_bf16 v[20:23], v[148:151], v[172:175], v[20:23]
	v_mfma_f32_16x16x32_bf16 v[16:19], v[152:155], v[168:171], v[16:19]
	s_nop 0
	v_mfma_f32_16x16x32_bf16 v[16:19], v[156:159], v[172:175], v[16:19]
	v_mfma_f32_16x16x32_bf16 v[12:15], v[144:147], v[176:179], v[12:15]
	s_nop 0
	v_mfma_f32_16x16x32_bf16 v[12:15], v[148:151], v[180:183], v[12:15]
	v_mfma_f32_16x16x32_bf16 v[8:11], v[152:155], v[176:179], v[8:11]
	s_nop 0
	v_mfma_f32_16x16x32_bf16 v[8:11], v[156:159], v[180:183], v[8:11]
	v_mfma_f32_16x16x32_bf16 v[4:7], v[144:147], v[184:187], v[4:7]
	s_nop 0
	v_mfma_f32_16x16x32_bf16 v[4:7], v[148:151], v[188:191], v[4:7]
	v_mfma_f32_16x16x32_bf16 v[0:3], v[152:155], v[184:187], v[0:3]
	s_nop 0
	v_mfma_f32_16x16x32_bf16 v[0:3], v[156:159], v[188:191], v[0:3]
	s_setprio 0
	s_barrier
	ds_read_b128 v[140:143], v203
	ds_read_b128 v[144:147], v204
	ds_read_b128 v[148:151], v205
	ds_read_b128 v[152:155], v206
	ds_read_b128 v[156:159], v207
	ds_read_b128 v[136:139], v208
	ds_read_b128 v[132:135], v209
	ds_read_b128 v[128:131], v210
	ds_read_b128 v[160:163], v197 offset:32768
	ds_read_b128 v[164:167], v197 offset:33792
	ds_read_b128 v[168:171], v197 offset:34816
	ds_read_b128 v[172:175], v197 offset:35840
	ds_read_b128 v[176:179], v197 offset:36864
	ds_read_b128 v[180:183], v197 offset:37888
	ds_read_b128 v[184:187], v197 offset:38912
	ds_read_b128 v[188:191], v197 offset:39936
	s_mov_b32 m0, s69
	s_add_i32 s91, s66, 0x20000
	buffer_load_dwordx4 v196, s[4:7], s91 offen lds
	s_add_i32 s91, s66, 0x30000
	s_mov_b32 m0, s70
	s_nop 0
	buffer_load_dwordx4 v196, s[4:7], s91 offen lds
	s_waitcnt vmcnt(8)
	s_waitcnt lgkmcnt(8)
	s_barrier
	s_setprio 1
	s_waitcnt lgkmcnt(7)
	v_mfma_f32_16x16x32_bf16 v[124:127], v[140:143], v[160:163], v[124:127]
	s_waitcnt lgkmcnt(6)
	v_mfma_f32_16x16x32_bf16 v[124:127], v[144:147], v[164:167], v[124:127]
	v_mfma_f32_16x16x32_bf16 v[120:123], v[148:151], v[160:163], v[120:123]
	s_nop 0
	v_mfma_f32_16x16x32_bf16 v[120:123], v[152:155], v[164:167], v[120:123]
	s_waitcnt lgkmcnt(5)
	v_mfma_f32_16x16x32_bf16 v[116:119], v[140:143], v[168:171], v[116:119]
	s_waitcnt lgkmcnt(4)
	v_mfma_f32_16x16x32_bf16 v[116:119], v[144:147], v[172:175], v[116:119]
	v_mfma_f32_16x16x32_bf16 v[112:115], v[148:151], v[168:171], v[112:115]
	s_nop 0
	v_mfma_f32_16x16x32_bf16 v[112:115], v[152:155], v[172:175], v[112:115]
	s_waitcnt lgkmcnt(3)
	v_mfma_f32_16x16x32_bf16 v[108:111], v[140:143], v[176:179], v[108:111]
	s_waitcnt lgkmcnt(2)
	v_mfma_f32_16x16x32_bf16 v[108:111], v[144:147], v[180:183], v[108:111]
	v_mfma_f32_16x16x32_bf16 v[104:107], v[148:151], v[176:179], v[104:107]
	s_nop 0
	v_mfma_f32_16x16x32_bf16 v[104:107], v[152:155], v[180:183], v[104:107]
	s_waitcnt lgkmcnt(1)
	v_mfma_f32_16x16x32_bf16 v[100:103], v[140:143], v[184:187], v[100:103]
	s_waitcnt lgkmcnt(0)
	v_mfma_f32_16x16x32_bf16 v[100:103], v[144:147], v[188:191], v[100:103]
	v_mfma_f32_16x16x32_bf16 v[96:99], v[148:151], v[184:187], v[96:99]
	s_nop 0
	v_mfma_f32_16x16x32_bf16 v[96:99], v[152:155], v[188:191], v[96:99]
	s_setprio 0
	s_setprio 1
	v_mfma_f32_16x16x32_bf16 v[92:95], v[156:159], v[160:163], v[92:95]
	s_nop 0
	v_mfma_f32_16x16x32_bf16 v[92:95], v[136:139], v[164:167], v[92:95]
	v_mfma_f32_16x16x32_bf16 v[88:91], v[132:135], v[160:163], v[88:91]
	s_nop 0
	v_mfma_f32_16x16x32_bf16 v[88:91], v[128:131], v[164:167], v[88:91]
	v_mfma_f32_16x16x32_bf16 v[84:87], v[156:159], v[168:171], v[84:87]
	s_nop 0
	v_mfma_f32_16x16x32_bf16 v[84:87], v[136:139], v[172:175], v[84:87]
	v_mfma_f32_16x16x32_bf16 v[80:83], v[132:135], v[168:171], v[80:83]
	s_nop 0
	v_mfma_f32_16x16x32_bf16 v[80:83], v[128:131], v[172:175], v[80:83]
	v_mfma_f32_16x16x32_bf16 v[76:79], v[156:159], v[176:179], v[76:79]
	s_nop 0
	v_mfma_f32_16x16x32_bf16 v[76:79], v[136:139], v[180:183], v[76:79]
	v_mfma_f32_16x16x32_bf16 v[72:75], v[132:135], v[176:179], v[72:75]
	s_nop 0
	v_mfma_f32_16x16x32_bf16 v[72:75], v[128:131], v[180:183], v[72:75]
	v_mfma_f32_16x16x32_bf16 v[68:71], v[156:159], v[184:187], v[68:71]
	s_nop 0
	v_mfma_f32_16x16x32_bf16 v[68:71], v[136:139], v[188:191], v[68:71]
	v_mfma_f32_16x16x32_bf16 v[64:67], v[132:135], v[184:187], v[64:67]
	s_nop 0
	v_mfma_f32_16x16x32_bf16 v[64:67], v[128:131], v[188:191], v[64:67]
	s_setprio 0
	s_barrier
	ds_read_b128 v[160:163], v197 offset:49152
	ds_read_b128 v[164:167], v197 offset:50176
	ds_read_b128 v[168:171], v197 offset:51200
	ds_read_b128 v[172:175], v197 offset:52224
	ds_read_b128 v[176:179], v197 offset:53248
	ds_read_b128 v[180:183], v197 offset:54272
	ds_read_b128 v[184:187], v197 offset:55296
	ds_read_b128 v[188:191], v197 offset:56320
	s_mov_b32 m0, s72
	s_add_i32 s91, s90, 0x80
	buffer_load_dwordx4 v192, s[8:11], s91 offen lds
	s_add_i32 s91, s90, 0x20080
	s_mov_b32 m0, s73
	s_add_i32 s66, s66, 0x10080
	buffer_load_dwordx4 v192, s[8:11], s91 offen lds
	s_add_i32 s91, s90, 0x2080
	s_mov_b32 m0, s76
	s_add_i32 s90, s90, 0x22080
	buffer_load_dwordx4 v192, s[8:11], s91 offen lds
	s_mov_b32 m0, s77
	s_nop 0
	buffer_load_dwordx4 v192, s[8:11], s90 offen lds
	s_mov_b32 m0, s74
	s_nop 0
	buffer_load_dwordx4 v196, s[4:7], s67 offen lds
	s_mov_b32 m0, s75
	s_nop 0
	buffer_load_dwordx4 v196, s[4:7], s66 offen lds
	s_waitcnt vmcnt(8)
	s_waitcnt lgkmcnt(6)
	s_barrier
	s_setprio 1
	s_waitcnt lgkmcnt(7)
	v_mfma_f32_16x16x32_bf16 v[60:63], v[140:143], v[160:163], v[60:63]
	s_waitcnt lgkmcnt(6)
	v_mfma_f32_16x16x32_bf16 v[60:63], v[144:147], v[164:167], v[60:63]
	v_mfma_f32_16x16x32_bf16 v[56:59], v[148:151], v[160:163], v[56:59]
	s_nop 0
	v_mfma_f32_16x16x32_bf16 v[56:59], v[152:155], v[164:167], v[56:59]
	s_waitcnt lgkmcnt(5)
	v_mfma_f32_16x16x32_bf16 v[52:55], v[140:143], v[168:171], v[52:55]
	s_waitcnt lgkmcnt(4)
	v_mfma_f32_16x16x32_bf16 v[52:55], v[144:147], v[172:175], v[52:55]
	v_mfma_f32_16x16x32_bf16 v[48:51], v[148:151], v[168:171], v[48:51]
	s_nop 0
	v_mfma_f32_16x16x32_bf16 v[48:51], v[152:155], v[172:175], v[48:51]
	s_waitcnt lgkmcnt(3)
	v_mfma_f32_16x16x32_bf16 v[44:47], v[140:143], v[176:179], v[44:47]
	s_waitcnt lgkmcnt(2)
	v_mfma_f32_16x16x32_bf16 v[44:47], v[144:147], v[180:183], v[44:47]
	v_mfma_f32_16x16x32_bf16 v[40:43], v[148:151], v[176:179], v[40:43]
	s_nop 0
	v_mfma_f32_16x16x32_bf16 v[40:43], v[152:155], v[180:183], v[40:43]
	s_waitcnt lgkmcnt(1)
	v_mfma_f32_16x16x32_bf16 v[36:39], v[140:143], v[184:187], v[36:39]
	s_waitcnt lgkmcnt(0)
	v_mfma_f32_16x16x32_bf16 v[36:39], v[144:147], v[188:191], v[36:39]
	v_mfma_f32_16x16x32_bf16 v[32:35], v[148:151], v[184:187], v[32:35]
	s_nop 0
	v_mfma_f32_16x16x32_bf16 v[32:35], v[152:155], v[188:191], v[32:35]
	s_setprio 0
	s_setprio 1
	v_mfma_f32_16x16x32_bf16 v[28:31], v[156:159], v[160:163], v[28:31]
	s_nop 0
	v_mfma_f32_16x16x32_bf16 v[28:31], v[136:139], v[164:167], v[28:31]
	v_mfma_f32_16x16x32_bf16 v[24:27], v[132:135], v[160:163], v[24:27]
	s_nop 0
	v_mfma_f32_16x16x32_bf16 v[24:27], v[128:131], v[164:167], v[24:27]
	v_mfma_f32_16x16x32_bf16 v[20:23], v[156:159], v[168:171], v[20:23]
	s_nop 0
	v_mfma_f32_16x16x32_bf16 v[20:23], v[136:139], v[172:175], v[20:23]
	v_mfma_f32_16x16x32_bf16 v[16:19], v[132:135], v[168:171], v[16:19]
	s_nop 0
	v_mfma_f32_16x16x32_bf16 v[16:19], v[128:131], v[172:175], v[16:19]
	v_mfma_f32_16x16x32_bf16 v[12:15], v[156:159], v[176:179], v[12:15]
	s_nop 0
	v_mfma_f32_16x16x32_bf16 v[12:15], v[136:139], v[180:183], v[12:15]
	v_mfma_f32_16x16x32_bf16 v[8:11], v[132:135], v[176:179], v[8:11]
	s_nop 0
	v_mfma_f32_16x16x32_bf16 v[8:11], v[128:131], v[180:183], v[8:11]
	v_mfma_f32_16x16x32_bf16 v[4:7], v[156:159], v[184:187], v[4:7]
	s_nop 0
	v_mfma_f32_16x16x32_bf16 v[4:7], v[136:139], v[188:191], v[4:7]
	v_mfma_f32_16x16x32_bf16 v[0:3], v[132:135], v[184:187], v[0:3]
	s_nop 0
	v_mfma_f32_16x16x32_bf16 v[0:3], v[128:131], v[188:191], v[0:3]
	s_setprio 0
	s_barrier
	s_add_i32 s43, s43, 2
	s_addk_i32 s33, 0x100
	s_addk_i32 s42, 0x100
	s_cmp_gt_u32 s43, 5
	s_cbranch_scc0 .LBB0_254
	s_and_b64 vcc, exec, s[14:15]
	s_cbranch_vccz .LBB0_257
	s_barrier

.LBB0_344:
	s_waitcnt lgkmcnt(0)
	s_add_i32 s4, s60, 0x180
	s_add_i32 s5, s36, 0x180
	s_barrier
	s_setprio 1
	s_waitcnt lgkmcnt(7)
	v_mfma_f32_16x16x32_bf16 v[60:63], v[164:167], v[196:199], 0
	s_waitcnt lgkmcnt(6)
	v_mfma_f32_16x16x32_bf16 v[60:63], v[160:163], v[192:195], v[60:63]
	v_mfma_f32_16x16x32_bf16 v[56:59], v[156:159], v[196:199], 0
	s_nop 0
	v_mfma_f32_16x16x32_bf16 v[56:59], v[152:155], v[192:195], v[56:59]
	s_waitcnt lgkmcnt(5)
	v_mfma_f32_16x16x32_bf16 v[52:55], v[164:167], v[188:191], 0
	s_waitcnt lgkmcnt(4)
	v_mfma_f32_16x16x32_bf16 v[52:55], v[160:163], v[184:187], v[52:55]
	v_mfma_f32_16x16x32_bf16 v[48:51], v[156:159], v[188:191], 0
	s_nop 0
	v_mfma_f32_16x16x32_bf16 v[48:51], v[152:155], v[184:187], v[48:51]
	s_waitcnt lgkmcnt(3)
	v_mfma_f32_16x16x32_bf16 v[44:47], v[164:167], v[180:183], 0
	s_waitcnt lgkmcnt(2)
	v_mfma_f32_16x16x32_bf16 v[44:47], v[160:163], v[176:179], v[44:47]
	v_mfma_f32_16x16x32_bf16 v[40:43], v[156:159], v[180:183], 0
	s_nop 0
	v_mfma_f32_16x16x32_bf16 v[40:43], v[152:155], v[176:179], v[40:43]
	s_waitcnt lgkmcnt(1)
	v_mfma_f32_16x16x32_bf16 v[36:39], v[164:167], v[172:175], 0
	s_waitcnt lgkmcnt(0)
	v_mfma_f32_16x16x32_bf16 v[36:39], v[160:163], v[168:171], v[36:39]
	v_mfma_f32_16x16x32_bf16 v[32:35], v[156:159], v[172:175], 0
	s_nop 0
	v_mfma_f32_16x16x32_bf16 v[32:35], v[152:155], v[168:171], v[32:35]
	s_setprio 0
	s_setprio 1
	v_mfma_f32_16x16x32_bf16 v[28:31], v[148:151], v[196:199], 0
	s_nop 0
	v_mfma_f32_16x16x32_bf16 v[28:31], v[144:147], v[192:195], v[28:31]
	v_mfma_f32_16x16x32_bf16 v[24:27], v[140:143], v[196:199], 0
	s_nop 0
	v_mfma_f32_16x16x32_bf16 v[24:27], v[136:139], v[192:195], v[24:27]
	v_mfma_f32_16x16x32_bf16 v[20:23], v[148:151], v[188:191], 0
	s_nop 0
	v_mfma_f32_16x16x32_bf16 v[20:23], v[144:147], v[184:187], v[20:23]
	v_mfma_f32_16x16x32_bf16 v[16:19], v[140:143], v[188:191], 0
	s_nop 0
	v_mfma_f32_16x16x32_bf16 v[16:19], v[136:139], v[184:187], v[16:19]
	v_mfma_f32_16x16x32_bf16 v[12:15], v[148:151], v[180:183], 0
	s_nop 0
	v_mfma_f32_16x16x32_bf16 v[12:15], v[144:147], v[176:179], v[12:15]
	v_mfma_f32_16x16x32_bf16 v[8:11], v[140:143], v[180:183], 0
	s_nop 0
	v_mfma_f32_16x16x32_bf16 v[8:11], v[136:139], v[176:179], v[8:11]
	v_mfma_f32_16x16x32_bf16 v[4:7], v[148:151], v[172:175], 0
	s_nop 0
	v_mfma_f32_16x16x32_bf16 v[4:7], v[144:147], v[168:171], v[4:7]
	v_mfma_f32_16x16x32_bf16 v[0:3], v[140:143], v[172:175], 0
	s_nop 0
	v_mfma_f32_16x16x32_bf16 v[0:3], v[136:139], v[168:171], v[0:3]
	s_setprio 0
	s_barrier
	ds_read_b128 v[164:167], v225
	ds_read_b128 v[160:163], v226
	ds_read_b128 v[156:159], v227
	ds_read_b128 v[152:155], v228
	ds_read_b128 v[148:151], v229
	ds_read_b128 v[144:147], v230
	ds_read_b128 v[140:143], v231
	ds_read_b128 v[136:139], v232
	ds_read_b128 v[168:171], v233 offset:32768
	ds_read_b128 v[172:175], v233 offset:33792
	ds_read_b128 v[176:179], v233 offset:34816
	ds_read_b128 v[180:183], v233 offset:35840
	ds_read_b128 v[184:187], v233 offset:36864
	ds_read_b128 v[188:191], v233 offset:37888
	ds_read_b128 v[192:195], v233 offset:38912
	ds_read_b128 v[196:199], v233 offset:39936
	s_mov_b32 m0, s72
	s_add_i32 s14, s60, 0x100100
	buffer_load_dwordx4 v214, s[8:11], s14 offen lds
	s_add_i32 s14, s60, 0x180100
	s_mov_b32 m0, s73
	s_nop 0
	buffer_load_dwordx4 v214, s[8:11], s14 offen lds
	s_waitcnt vmcnt(10)
	s_waitcnt lgkmcnt(8)
	s_barrier
	s_setprio 1
	s_waitcnt lgkmcnt(7)
	v_mfma_f32_16x16x32_bf16 v[124:127], v[164:167], v[168:171], v[124:127]
	s_waitcnt lgkmcnt(6)
	v_mfma_f32_16x16x32_bf16 v[124:127], v[160:163], v[172:175], v[124:127]
	v_mfma_f32_16x16x32_bf16 v[120:123], v[156:159], v[168:171], v[120:123]
	s_nop 0
	v_mfma_f32_16x16x32_bf16 v[120:123], v[152:155], v[172:175], v[120:123]
	s_waitcnt lgkmcnt(5)
	v_mfma_f32_16x16x32_bf16 v[116:119], v[164:167], v[176:179], v[116:119]
	s_waitcnt lgkmcnt(4)
	v_mfma_f32_16x16x32_bf16 v[116:119], v[160:163], v[180:183], v[116:119]
	v_mfma_f32_16x16x32_bf16 v[112:115], v[156:159], v[176:179], v[112:115]
	s_nop 0
	v_mfma_f32_16x16x32_bf16 v[112:115], v[152:155], v[180:183], v[112:115]
	s_waitcnt lgkmcnt(3)
	v_mfma_f32_16x16x32_bf16 v[108:111], v[164:167], v[184:187], v[108:111]
	s_waitcnt lgkmcnt(2)
	v_mfma_f32_16x16x32_bf16 v[108:111], v[160:163], v[188:191], v[108:111]
	v_mfma_f32_16x16x32_bf16 v[104:107], v[156:159], v[184:187], v[104:107]
	s_nop 0
	v_mfma_f32_16x16x32_bf16 v[104:107], v[152:155], v[188:191], v[104:107]
	s_waitcnt lgkmcnt(1)
	v_mfma_f32_16x16x32_bf16 v[100:103], v[164:167], v[192:195], v[100:103]
	s_waitcnt lgkmcnt(0)
	v_mfma_f32_16x16x32_bf16 v[100:103], v[160:163], v[196:199], v[100:103]
	v_mfma_f32_16x16x32_bf16 v[96:99], v[156:159], v[192:195], v[96:99]
	s_nop 0
	v_mfma_f32_16x16x32_bf16 v[96:99], v[152:155], v[196:199], v[96:99]
	s_setprio 0
	s_setprio 1
	v_mfma_f32_16x16x32_bf16 v[92:95], v[148:151], v[168:171], v[92:95]
	s_nop 0
	v_mfma_f32_16x16x32_bf16 v[92:95], v[144:147], v[172:175], v[92:95]
	v_mfma_f32_16x16x32_bf16 v[88:91], v[140:143], v[168:171], v[88:91]
	s_nop 0
	v_mfma_f32_16x16x32_bf16 v[88:91], v[136:139], v[172:175], v[88:91]
	v_mfma_f32_16x16x32_bf16 v[84:87], v[148:151], v[176:179], v[84:87]
	s_nop 0
	v_mfma_f32_16x16x32_bf16 v[84:87], v[144:147], v[180:183], v[84:87]
	v_mfma_f32_16x16x32_bf16 v[80:83], v[140:143], v[176:179], v[80:83]
	s_nop 0
	v_mfma_f32_16x16x32_bf16 v[80:83], v[136:139], v[180:183], v[80:83]
	v_mfma_f32_16x16x32_bf16 v[76:79], v[148:151], v[184:187], v[76:79]
	s_nop 0
	v_mfma_f32_16x16x32_bf16 v[76:79], v[144:147], v[188:191], v[76:79]
	v_mfma_f32_16x16x32_bf16 v[72:75], v[140:143], v[184:187], v[72:75]
	s_nop 0
	v_mfma_f32_16x16x32_bf16 v[72:75], v[136:139], v[188:191], v[72:75]
	v_mfma_f32_16x16x32_bf16 v[68:71], v[148:151], v[192:195], v[68:71]
	s_nop 0
	v_mfma_f32_16x16x32_bf16 v[68:71], v[144:147], v[196:199], v[68:71]
	v_mfma_f32_16x16x32_bf16 v[64:67], v[140:143], v[192:195], v[64:67]
	s_nop 0
	v_mfma_f32_16x16x32_bf16 v[64:67], v[136:139], v[196:199], v[64:67]
	s_setprio 0
	s_barrier
	ds_read_b128 v[168:171], v233 offset:49152
	ds_read_b128 v[172:175], v233 offset:50176
	ds_read_b128 v[176:179], v233 offset:51200
	ds_read_b128 v[180:183], v233 offset:52224
	ds_read_b128 v[184:187], v233 offset:53248
	ds_read_b128 v[188:191], v233 offset:54272
	ds_read_b128 v[192:195], v233 offset:55296
	ds_read_b128 v[196:199], v233 offset:56320
	s_mov_b32 m0, s76
	s_mov_b32 s14, s10
	s_mov_b32 s15, s11
	buffer_load_dwordx4 v215, s[12:15], s5 offen lds
	s_add_i32 s5, s36, 0x100180
	s_mov_b32 m0, s77
	s_nop 0
	buffer_load_dwordx4 v215, s[12:15], s5 offen lds
	s_add_i32 s5, s36, 0x10180
	s_mov_b32 m0, s80
	s_nop 0
	buffer_load_dwordx4 v215, s[12:15], s5 offen lds
	s_add_i32 s5, s36, 0x110180
	s_mov_b32 m0, s81
	s_nop 0
	buffer_load_dwordx4 v215, s[12:15], s5 offen lds
	s_mov_b32 m0, s78
	s_nop 0
	buffer_load_dwordx4 v214, s[8:11], s4 offen lds
	s_add_i32 s4, s60, 0x80180
	s_mov_b32 m0, s79
	s_nop 0
	buffer_load_dwordx4 v214, s[8:11], s4 offen lds
	s_waitcnt vmcnt(8)
	s_waitcnt lgkmcnt(6)
	s_barrier
	s_setprio 1
	s_waitcnt lgkmcnt(7)
	v_mfma_f32_16x16x32_bf16 v[60:63], v[164:167], v[168:171], v[60:63]
	s_waitcnt lgkmcnt(6)
	v_mfma_f32_16x16x32_bf16 v[60:63], v[160:163], v[172:175], v[60:63]
	v_mfma_f32_16x16x32_bf16 v[56:59], v[156:159], v[168:171], v[56:59]
	s_nop 0
	v_mfma_f32_16x16x32_bf16 v[56:59], v[152:155], v[172:175], v[56:59]
	s_waitcnt lgkmcnt(5)
	v_mfma_f32_16x16x32_bf16 v[52:55], v[164:167], v[176:179], v[52:55]
	s_waitcnt lgkmcnt(4)
	v_mfma_f32_16x16x32_bf16 v[52:55], v[160:163], v[180:183], v[52:55]
	v_mfma_f32_16x16x32_bf16 v[48:51], v[156:159], v[176:179], v[48:51]
	s_nop 0
	v_mfma_f32_16x16x32_bf16 v[48:51], v[152:155], v[180:183], v[48:51]
	s_waitcnt lgkmcnt(3)
	v_mfma_f32_16x16x32_bf16 v[44:47], v[164:167], v[184:187], v[44:47]
	s_waitcnt lgkmcnt(2)
	v_mfma_f32_16x16x32_bf16 v[44:47], v[160:163], v[188:191], v[44:47]
	v_mfma_f32_16x16x32_bf16 v[40:43], v[156:159], v[184:187], v[40:43]
	s_nop 0
	v_mfma_f32_16x16x32_bf16 v[40:43], v[152:155], v[188:191], v[40:43]
	s_waitcnt lgkmcnt(1)
	v_mfma_f32_16x16x32_bf16 v[36:39], v[164:167], v[192:195], v[36:39]
	s_waitcnt lgkmcnt(0)
	v_mfma_f32_16x16x32_bf16 v[36:39], v[160:163], v[196:199], v[36:39]
	v_mfma_f32_16x16x32_bf16 v[32:35], v[156:159], v[192:195], v[32:35]
	s_nop 0
	v_mfma_f32_16x16x32_bf16 v[32:35], v[152:155], v[196:199], v[32:35]
	s_setprio 0
	s_setprio 1
	v_mfma_f32_16x16x32_bf16 v[28:31], v[148:151], v[168:171], v[28:31]
	s_nop 0
	v_mfma_f32_16x16x32_bf16 v[28:31], v[144:147], v[172:175], v[28:31]
	v_mfma_f32_16x16x32_bf16 v[24:27], v[140:143], v[168:171], v[24:27]
	s_nop 0
	v_mfma_f32_16x16x32_bf16 v[24:27], v[136:139], v[172:175], v[24:27]
	v_mfma_f32_16x16x32_bf16 v[20:23], v[148:151], v[176:179], v[20:23]
	s_nop 0
	v_mfma_f32_16x16x32_bf16 v[20:23], v[144:147], v[180:183], v[20:23]
	v_mfma_f32_16x16x32_bf16 v[16:19], v[140:143], v[176:179], v[16:19]
	s_nop 0
	v_mfma_f32_16x16x32_bf16 v[16:19], v[136:139], v[180:183], v[16:19]
	v_mfma_f32_16x16x32_bf16 v[12:15], v[148:151], v[184:187], v[12:15]
	s_nop 0
	v_mfma_f32_16x16x32_bf16 v[12:15], v[144:147], v[188:191], v[12:15]
	v_mfma_f32_16x16x32_bf16 v[8:11], v[140:143], v[184:187], v[8:11]
	s_nop 0
	v_mfma_f32_16x16x32_bf16 v[8:11], v[136:139], v[188:191], v[8:11]
	v_mfma_f32_16x16x32_bf16 v[4:7], v[148:151], v[192:195], v[4:7]
	s_nop 0
	v_mfma_f32_16x16x32_bf16 v[4:7], v[144:147], v[196:199], v[4:7]
	v_mfma_f32_16x16x32_bf16 v[0:3], v[140:143], v[192:195], v[0:3]
	s_nop 0
	v_mfma_f32_16x16x32_bf16 v[0:3], v[136:139], v[196:199], v[0:3]
	s_setprio 0
	s_barrier
	s_waitcnt vmcnt(14)
	v_mul_f32_e32 v132, 0x42800000, v132
	v_mul_f32_e32 v128, 0x42800000, v128
	v_mul_f32_e32 v133, 0x42800000, v133
	v_mul_f32_e32 v129, 0x42800000, v129
	v_mul_f32_e32 v134, 0x42800000, v134
	v_mul_f32_e32 v130, 0x42800000, v130
	v_mul_f32_e32 v135, 0x42800000, v135
	v_mul_f32_e32 v131, 0x42800000, v131
	v_cvt_pk_fp8_f32 v204, v128, v132
	v_cvt_pk_fp8_f32 v234, v129, v133
	v_cvt_pk_fp8_f32 v235, v130, v134
	v_cvt_pk_fp8_f32 v236, v131, v135
	s_add_i32 s33, s36, 0x200
	s_mov_b32 s61, 0
	s_mov_b32 s66, s75
	s_mov_b32 s94, s86
	s_branch .LBB0_347

.LBB0_347:
	v_mov_b32_e32 v152, v204
	v_mov_b32_e32 v153, v234
	v_mov_b32_e32 v154, v235
	v_mov_b32_e32 v155, v236
	ds_read_b128 v[158:161], v217
	ds_read_b128 v[162:165], v218
	ds_read_b128 v[166:169], v219
	ds_read_b128 v[170:173], v220
	ds_read_b128 v[148:151], v221
	ds_read_b128 v[144:147], v222
	ds_read_b128 v[140:143], v223
	ds_read_b128 v[136:139], v224
	ds_read_b128 v[174:177], v233
	ds_read_b128 v[178:181], v233 offset:1024
	ds_read_b128 v[182:185], v233 offset:2048
	ds_read_b128 v[186:189], v233 offset:3072
	ds_read_b128 v[190:193], v233 offset:4096
	ds_read_b128 v[194:197], v233 offset:5120
	ds_read_b128 v[234:237], v233 offset:6144
	ds_read_b128 v[238:241], v233 offset:7168
	s_add_i32 s4, s60, s61
	s_mov_b32 s46, s94
	s_add_i32 s94, s94, 1
	s_add_i32 s5, s4, 0x200
	s_add_i32 s16, s33, s61
	s_cmpk_eq_i32 s61, 0x1e00
	s_cselect_b32 s47, s90, s5
	s_cselect_b32 s97, s91, s16
	s_add_i32 s96, s47, 0x80
	s_mov_b32 m0, s82
	s_add_i32 s5, s4, 0x100180
	buffer_load_dwordx4 v214, s[8:11], s5 offen lds
	s_add_i32 s4, s4, 0x180180
	s_mov_b32 m0, s85
	s_add_i32 vcc_lo, s97, 0x80
	buffer_load_dwordx4 v214, s[8:11], s4 offen lds
	s_lshr_b32 s4, s94, 2
	s_mul_i32 s5, s4, s34
	s_add_i32 s16, s5, s2
	s_cmp_lt_i32 s4, s3
	s_cselect_b64 s[4:5], -1, 0
	s_and_b64 s[44:45], s[4:5], exec
	s_cselect_b32 s16, s16, 0
	s_bfe_u32 s17, s94, 0x10001
	s_or_b32 s17, s17, s83
	s_bfe_u32 s67, s16, 0x50007
	s_bfe_u32 s36, s16, 0x50002
	s_and_b32 s95, s16, 3
	s_cmpk_gt_i32 s16, 0xfff
	s_cselect_b64 s[44:45], -1, 0
	v_lshl_or_b32 v156, s17, 3, v216
	s_and_b64 s[16:17], s[44:45], exec
	s_cselect_b32 s16, s25, s21
	s_cselect_b32 s17, s24, s20
	s_lshl_b32 vcc_hi, s67, 23
	s_add_u32 s17, s17, vcc_hi
	s_addc_u32 s16, s16, 0
	s_lshl_b32 vcc_hi, s36, 18
	s_add_u32 s17, s17, vcc_hi
	s_addc_u32 vcc_hi, s16, 0
	s_lshl_b32 s16, s95, 9
	s_add_u32 s16, s17, s16
	v_and_or_b32 v204, s66, 2, v200
	s_addc_u32 s17, vcc_hi, 0
	v_lshlrev_b64 v[128:129], 11, v[204:205]
	v_lshl_add_u64 v[128:129], s[16:17], 0, v[128:129]
	v_lshlrev_b32_e32 v204, 4, v156
	v_lshl_add_u64 v[132:133], v[128:129], 0, v[204:205]
	global_load_dwordx4 v[128:131], v[132:133], off nt
	s_nop 0
	global_load_dwordx4 v[132:135], v[132:133], off offset:2048 nt
	s_waitcnt vmcnt(10)
	s_waitcnt lgkmcnt(8)
	s_barrier
	s_setprio 1
	s_waitcnt lgkmcnt(7)
	v_mfma_f32_16x16x32_bf16 v[124:127], v[158:161], v[174:177], v[124:127]
	s_waitcnt lgkmcnt(6)
	v_mfma_f32_16x16x32_bf16 v[124:127], v[162:165], v[178:181], v[124:127]
	v_mfma_f32_16x16x32_bf16 v[120:123], v[166:169], v[174:177], v[120:123]
	s_nop 0
	v_mfma_f32_16x16x32_bf16 v[120:123], v[170:173], v[178:181], v[120:123]
	s_waitcnt lgkmcnt(5)
	v_mfma_f32_16x16x32_bf16 v[116:119], v[158:161], v[182:185], v[116:119]
	s_waitcnt lgkmcnt(4)
	v_mfma_f32_16x16x32_bf16 v[116:119], v[162:165], v[186:189], v[116:119]
	v_mfma_f32_16x16x32_bf16 v[112:115], v[166:169], v[182:185], v[112:115]
	s_nop 0
	v_mfma_f32_16x16x32_bf16 v[112:115], v[170:173], v[186:189], v[112:115]
	s_waitcnt lgkmcnt(3)
	v_mfma_f32_16x16x32_bf16 v[108:111], v[158:161], v[190:193], v[108:111]
	s_waitcnt lgkmcnt(2)
	v_mfma_f32_16x16x32_bf16 v[108:111], v[162:165], v[194:197], v[108:111]
	v_mfma_f32_16x16x32_bf16 v[104:107], v[166:169], v[190:193], v[104:107]
	s_nop 0
	v_mfma_f32_16x16x32_bf16 v[104:107], v[170:173], v[194:197], v[104:107]
	s_waitcnt lgkmcnt(1)
	v_mfma_f32_16x16x32_bf16 v[100:103], v[158:161], v[234:237], v[100:103]
	s_waitcnt lgkmcnt(0)
	v_mfma_f32_16x16x32_bf16 v[100:103], v[162:165], v[238:241], v[100:103]
	v_mfma_f32_16x16x32_bf16 v[96:99], v[166:169], v[234:237], v[96:99]
	s_nop 0
	v_mfma_f32_16x16x32_bf16 v[96:99], v[170:173], v[238:241], v[96:99]
	s_setprio 0
	s_setprio 1
	v_mfma_f32_16x16x32_bf16 v[92:95], v[148:151], v[174:177], v[92:95]
	s_nop 0
	v_mfma_f32_16x16x32_bf16 v[92:95], v[144:147], v[178:181], v[92:95]
	v_mfma_f32_16x16x32_bf16 v[88:91], v[140:143], v[174:177], v[88:91]
	s_nop 0
	v_mfma_f32_16x16x32_bf16 v[88:91], v[136:139], v[178:181], v[88:91]
	v_mfma_f32_16x16x32_bf16 v[84:87], v[148:151], v[182:185], v[84:87]
	s_nop 0
	v_mfma_f32_16x16x32_bf16 v[84:87], v[144:147], v[186:189], v[84:87]
	v_mfma_f32_16x16x32_bf16 v[80:83], v[140:143], v[182:185], v[80:83]
	s_nop 0
	v_mfma_f32_16x16x32_bf16 v[80:83], v[136:139], v[186:189], v[80:83]
	v_mfma_f32_16x16x32_bf16 v[76:79], v[148:151], v[190:193], v[76:79]
	s_nop 0
	v_mfma_f32_16x16x32_bf16 v[76:79], v[144:147], v[194:197], v[76:79]
	v_mfma_f32_16x16x32_bf16 v[72:75], v[140:143], v[190:193], v[72:75]
	s_nop 0
	v_mfma_f32_16x16x32_bf16 v[72:75], v[136:139], v[194:197], v[72:75]
	v_mfma_f32_16x16x32_bf16 v[68:71], v[148:151], v[234:237], v[68:71]
	s_nop 0
	v_mfma_f32_16x16x32_bf16 v[68:71], v[144:147], v[238:241], v[68:71]
	v_mfma_f32_16x16x32_bf16 v[64:67], v[140:143], v[234:237], v[64:67]
	s_nop 0
	v_mfma_f32_16x16x32_bf16 v[64:67], v[136:139], v[238:241], v[64:67]
	s_setprio 0
	s_barrier
	ds_read_b128 v[174:177], v233 offset:16384
	ds_read_b128 v[178:181], v233 offset:17408
	ds_read_b128 v[182:185], v233 offset:18432
	ds_read_b128 v[186:189], v233 offset:19456
	ds_read_b128 v[190:193], v233 offset:20480
	ds_read_b128 v[194:197], v233 offset:21504
	ds_read_b128 v[234:237], v233 offset:22528
	ds_read_b128 v[238:241], v233 offset:23552
	s_mov_b32 m0, s65
	s_add_i32 s16, s97, 0x100000
	buffer_load_dwordx4 v215, s[12:15], s97 offen lds
	s_mov_b32 m0, s68
	s_nop 0
	buffer_load_dwordx4 v215, s[12:15], s16 offen lds
	s_add_i32 s16, s97, 0x10000
	s_mov_b32 m0, s69
	s_nop 0
	buffer_load_dwordx4 v215, s[12:15], s16 offen lds
	s_add_i32 s16, s97, 0x110000
	s_mov_b32 m0, s70
	s_nop 0
	buffer_load_dwordx4 v215, s[12:15], s16 offen lds
	s_mov_b32 m0, s64
	s_add_i32 s16, s47, 0x80000
	buffer_load_dwordx4 v214, s[8:11], s47 offen lds
	s_mov_b32 m0, s71
	s_nop 0
	buffer_load_dwordx4 v214, s[8:11], s16 offen lds
	s_waitcnt vmcnt(10)
	s_waitcnt lgkmcnt(6)
	s_barrier
	s_setprio 1
	s_waitcnt lgkmcnt(7)
	v_mfma_f32_16x16x32_bf16 v[60:63], v[158:161], v[174:177], v[60:63]
	s_waitcnt lgkmcnt(6)
	v_mfma_f32_16x16x32_bf16 v[60:63], v[162:165], v[178:181], v[60:63]
	v_mfma_f32_16x16x32_bf16 v[56:59], v[166:169], v[174:177], v[56:59]
	s_nop 0
	v_mfma_f32_16x16x32_bf16 v[56:59], v[170:173], v[178:181], v[56:59]
	s_waitcnt lgkmcnt(5)
	v_mfma_f32_16x16x32_bf16 v[52:55], v[158:161], v[182:185], v[52:55]
	s_waitcnt lgkmcnt(4)
	v_mfma_f32_16x16x32_bf16 v[52:55], v[162:165], v[186:189], v[52:55]
	v_mfma_f32_16x16x32_bf16 v[48:51], v[166:169], v[182:185], v[48:51]
	s_nop 0
	v_mfma_f32_16x16x32_bf16 v[48:51], v[170:173], v[186:189], v[48:51]
	s_waitcnt lgkmcnt(3)
	v_mfma_f32_16x16x32_bf16 v[44:47], v[158:161], v[190:193], v[44:47]
	s_waitcnt lgkmcnt(2)
	v_mfma_f32_16x16x32_bf16 v[44:47], v[162:165], v[194:197], v[44:47]
	v_mfma_f32_16x16x32_bf16 v[40:43], v[166:169], v[190:193], v[40:43]
	s_nop 0
	v_mfma_f32_16x16x32_bf16 v[40:43], v[170:173], v[194:197], v[40:43]
	s_waitcnt lgkmcnt(1)
	v_mfma_f32_16x16x32_bf16 v[36:39], v[158:161], v[234:237], v[36:39]
	s_waitcnt lgkmcnt(0)
	v_mfma_f32_16x16x32_bf16 v[36:39], v[162:165], v[238:241], v[36:39]
	v_mfma_f32_16x16x32_bf16 v[32:35], v[166:169], v[234:237], v[32:35]
	s_nop 0
	v_mfma_f32_16x16x32_bf16 v[32:35], v[170:173], v[238:241], v[32:35]
	s_setprio 0
	s_setprio 1
	v_mfma_f32_16x16x32_bf16 v[28:31], v[148:151], v[174:177], v[28:31]
	s_nop 0
	v_mfma_f32_16x16x32_bf16 v[28:31], v[144:147], v[178:181], v[28:31]
	v_mfma_f32_16x16x32_bf16 v[24:27], v[140:143], v[174:177], v[24:27]
	s_nop 0
	v_mfma_f32_16x16x32_bf16 v[24:27], v[136:139], v[178:181], v[24:27]
	v_mfma_f32_16x16x32_bf16 v[20:23], v[148:151], v[182:185], v[20:23]
	s_nop 0
	v_mfma_f32_16x16x32_bf16 v[20:23], v[144:147], v[186:189], v[20:23]
	v_mfma_f32_16x16x32_bf16 v[16:19], v[140:143], v[182:185], v[16:19]
	s_nop 0
	v_mfma_f32_16x16x32_bf16 v[16:19], v[136:139], v[186:189], v[16:19]
	v_mfma_f32_16x16x32_bf16 v[12:15], v[148:151], v[190:193], v[12:15]
	s_nop 0
	v_mfma_f32_16x16x32_bf16 v[12:15], v[144:147], v[194:197], v[12:15]
	v_mfma_f32_16x16x32_bf16 v[8:11], v[140:143], v[190:193], v[8:11]
	s_nop 0
	v_mfma_f32_16x16x32_bf16 v[8:11], v[136:139], v[194:197], v[8:11]
	v_mfma_f32_16x16x32_bf16 v[4:7], v[148:151], v[234:237], v[4:7]
	s_nop 0
	v_mfma_f32_16x16x32_bf16 v[4:7], v[144:147], v[238:241], v[4:7]
	v_mfma_f32_16x16x32_bf16 v[0:3], v[140:143], v[234:237], v[0:3]
	s_nop 0
	v_mfma_f32_16x16x32_bf16 v[0:3], v[136:139], v[238:241], v[0:3]
	s_setprio 0
	s_barrier
	ds_read_b128 v[136:139], v225
	ds_read_b128 v[140:143], v226
	ds_read_b128 v[144:147], v227
	ds_read_b128 v[148:151], v228
	ds_read_b128 v[158:161], v229
	ds_read_b128 v[162:165], v230
	ds_read_b128 v[166:169], v231
	ds_read_b128 v[170:173], v232
	ds_read_b128 v[174:177], v233 offset:32768
	ds_read_b128 v[178:181], v233 offset:33792
	ds_read_b128 v[182:185], v233 offset:34816
	ds_read_b128 v[186:189], v233 offset:35840
	ds_read_b128 v[190:193], v233 offset:36864
	ds_read_b128 v[194:197], v233 offset:37888
	ds_read_b128 v[234:237], v233 offset:38912
	ds_read_b128 v[238:241], v233 offset:39936
	s_mov_b32 m0, s72
	s_add_i32 s16, s47, 0x100000
	buffer_load_dwordx4 v214, s[8:11], s16 offen lds
	s_add_i32 s16, s47, 0x180000
	s_mov_b32 m0, s73
	s_nop 0
	buffer_load_dwordx4 v214, s[8:11], s16 offen lds
	s_waitcnt vmcnt(10)
	s_waitcnt lgkmcnt(8)
	s_barrier
	s_setprio 1
	s_waitcnt lgkmcnt(7)
	v_mfma_f32_16x16x32_bf16 v[124:127], v[136:139], v[174:177], v[124:127]
	s_waitcnt lgkmcnt(6)
	v_mfma_f32_16x16x32_bf16 v[124:127], v[140:143], v[178:181], v[124:127]
	v_mfma_f32_16x16x32_bf16 v[120:123], v[144:147], v[174:177], v[120:123]
	s_nop 0
	v_mfma_f32_16x16x32_bf16 v[120:123], v[148:151], v[178:181], v[120:123]
	s_waitcnt lgkmcnt(5)
	v_mfma_f32_16x16x32_bf16 v[116:119], v[136:139], v[182:185], v[116:119]
	s_waitcnt lgkmcnt(4)
	v_mfma_f32_16x16x32_bf16 v[116:119], v[140:143], v[186:189], v[116:119]
	v_mfma_f32_16x16x32_bf16 v[112:115], v[144:147], v[182:185], v[112:115]
	s_nop 0
	v_mfma_f32_16x16x32_bf16 v[112:115], v[148:151], v[186:189], v[112:115]
	s_waitcnt lgkmcnt(3)
	v_mfma_f32_16x16x32_bf16 v[108:111], v[136:139], v[190:193], v[108:111]
	s_waitcnt lgkmcnt(2)
	v_mfma_f32_16x16x32_bf16 v[108:111], v[140:143], v[194:197], v[108:111]
	v_mfma_f32_16x16x32_bf16 v[104:107], v[144:147], v[190:193], v[104:107]
	s_nop 0
	v_mfma_f32_16x16x32_bf16 v[104:107], v[148:151], v[194:197], v[104:107]
	s_waitcnt lgkmcnt(1)
	v_mfma_f32_16x16x32_bf16 v[100:103], v[136:139], v[234:237], v[100:103]
	s_waitcnt lgkmcnt(0)
	v_mfma_f32_16x16x32_bf16 v[100:103], v[140:143], v[238:241], v[100:103]
	v_mfma_f32_16x16x32_bf16 v[96:99], v[144:147], v[234:237], v[96:99]
	s_nop 0
	v_mfma_f32_16x16x32_bf16 v[96:99], v[148:151], v[238:241], v[96:99]
	s_setprio 0
	s_setprio 1
	v_mfma_f32_16x16x32_bf16 v[92:95], v[158:161], v[174:177], v[92:95]
	s_nop 0
	v_mfma_f32_16x16x32_bf16 v[92:95], v[162:165], v[178:181], v[92:95]
	v_mfma_f32_16x16x32_bf16 v[88:91], v[166:169], v[174:177], v[88:91]
	s_nop 0
	v_mfma_f32_16x16x32_bf16 v[88:91], v[170:173], v[178:181], v[88:91]
	v_mfma_f32_16x16x32_bf16 v[84:87], v[158:161], v[182:185], v[84:87]
	s_nop 0
	v_mfma_f32_16x16x32_bf16 v[84:87], v[162:165], v[186:189], v[84:87]
	v_mfma_f32_16x16x32_bf16 v[80:83], v[166:169], v[182:185], v[80:83]
	s_nop 0
	v_mfma_f32_16x16x32_bf16 v[80:83], v[170:173], v[186:189], v[80:83]
	v_mfma_f32_16x16x32_bf16 v[76:79], v[158:161], v[190:193], v[76:79]
	s_nop 0
	v_mfma_f32_16x16x32_bf16 v[76:79], v[162:165], v[194:197], v[76:79]
	v_mfma_f32_16x16x32_bf16 v[72:75], v[166:169], v[190:193], v[72:75]
	s_nop 0
	v_mfma_f32_16x16x32_bf16 v[72:75], v[170:173], v[194:197], v[72:75]
	v_mfma_f32_16x16x32_bf16 v[68:71], v[158:161], v[234:237], v[68:71]
	s_nop 0
	v_mfma_f32_16x16x32_bf16 v[68:71], v[162:165], v[238:241], v[68:71]
	v_mfma_f32_16x16x32_bf16 v[64:67], v[166:169], v[234:237], v[64:67]
	s_nop 0
	v_mfma_f32_16x16x32_bf16 v[64:67], v[170:173], v[238:241], v[64:67]
	s_setprio 0
	s_barrier
	ds_read_b128 v[174:177], v233 offset:49152
	ds_read_b128 v[178:181], v233 offset:50176
	ds_read_b128 v[182:185], v233 offset:51200
	ds_read_b128 v[186:189], v233 offset:52224
	ds_read_b128 v[190:193], v233 offset:53248
	ds_read_b128 v[194:197], v233 offset:54272
	ds_read_b128 v[234:237], v233 offset:55296
	ds_read_b128 v[238:241], v233 offset:56320
	s_mov_b32 m0, s76
	s_add_i32 s16, s97, 0x100080
	buffer_load_dwordx4 v215, s[12:15], vcc_lo offen lds
	s_mov_b32 m0, s77
	s_add_i32 s47, s47, 0x80080
	buffer_load_dwordx4 v215, s[12:15], s16 offen lds
	s_add_i32 s16, s97, 0x10080
	s_mov_b32 m0, s80
	s_add_i32 s97, s97, 0x110080
	buffer_load_dwordx4 v215, s[12:15], s16 offen lds
	s_mov_b32 m0, s81
	s_nop 0
	buffer_load_dwordx4 v215, s[12:15], s97 offen lds
	s_mov_b32 m0, s78
	s_nop 0
	buffer_load_dwordx4 v214, s[8:11], s96 offen lds
	s_mov_b32 m0, s79
	s_nop 0
	buffer_load_dwordx4 v214, s[8:11], s47 offen lds
	s_waitcnt vmcnt(8)
	s_waitcnt lgkmcnt(6)
	s_barrier
	s_setprio 1
	s_waitcnt lgkmcnt(7)
	v_mfma_f32_16x16x32_bf16 v[60:63], v[136:139], v[174:177], v[60:63]
	s_waitcnt lgkmcnt(6)
	v_mfma_f32_16x16x32_bf16 v[60:63], v[140:143], v[178:181], v[60:63]
	v_mfma_f32_16x16x32_bf16 v[56:59], v[144:147], v[174:177], v[56:59]
	s_nop 0
	v_mfma_f32_16x16x32_bf16 v[56:59], v[148:151], v[178:181], v[56:59]
	s_waitcnt lgkmcnt(5)
	v_mfma_f32_16x16x32_bf16 v[52:55], v[136:139], v[182:185], v[52:55]
	s_waitcnt lgkmcnt(4)
	v_mfma_f32_16x16x32_bf16 v[52:55], v[140:143], v[186:189], v[52:55]
	v_mfma_f32_16x16x32_bf16 v[48:51], v[144:147], v[182:185], v[48:51]
	s_nop 0
	v_mfma_f32_16x16x32_bf16 v[48:51], v[148:151], v[186:189], v[48:51]
	s_waitcnt lgkmcnt(3)
	v_mfma_f32_16x16x32_bf16 v[44:47], v[136:139], v[190:193], v[44:47]
	s_waitcnt lgkmcnt(2)
	v_mfma_f32_16x16x32_bf16 v[44:47], v[140:143], v[194:197], v[44:47]
	v_mfma_f32_16x16x32_bf16 v[40:43], v[144:147], v[190:193], v[40:43]
	s_nop 0
	v_mfma_f32_16x16x32_bf16 v[40:43], v[148:151], v[194:197], v[40:43]
	s_waitcnt lgkmcnt(1)
	v_mfma_f32_16x16x32_bf16 v[36:39], v[136:139], v[234:237], v[36:39]
	s_waitcnt lgkmcnt(0)
	v_mfma_f32_16x16x32_bf16 v[36:39], v[140:143], v[238:241], v[36:39]
	v_mfma_f32_16x16x32_bf16 v[32:35], v[144:147], v[234:237], v[32:35]
	s_nop 0
	v_mfma_f32_16x16x32_bf16 v[32:35], v[148:151], v[238:241], v[32:35]
	s_setprio 0
	s_setprio 1
	v_mfma_f32_16x16x32_bf16 v[28:31], v[158:161], v[174:177], v[28:31]
	s_nop 0
	v_mfma_f32_16x16x32_bf16 v[28:31], v[162:165], v[178:181], v[28:31]
	v_mfma_f32_16x16x32_bf16 v[24:27], v[166:169], v[174:177], v[24:27]
	s_nop 0
	v_mfma_f32_16x16x32_bf16 v[24:27], v[170:173], v[178:181], v[24:27]
	v_mfma_f32_16x16x32_bf16 v[20:23], v[158:161], v[182:185], v[20:23]
	s_nop 0
	v_mfma_f32_16x16x32_bf16 v[20:23], v[162:165], v[186:189], v[20:23]
	v_mfma_f32_16x16x32_bf16 v[16:19], v[166:169], v[182:185], v[16:19]
	s_nop 0
	v_mfma_f32_16x16x32_bf16 v[16:19], v[170:173], v[186:189], v[16:19]
	v_mfma_f32_16x16x32_bf16 v[12:15], v[158:161], v[190:193], v[12:15]
	s_nop 0
	v_mfma_f32_16x16x32_bf16 v[12:15], v[162:165], v[194:197], v[12:15]
	v_mfma_f32_16x16x32_bf16 v[8:11], v[166:169], v[190:193], v[8:11]
	s_nop 0
	v_mfma_f32_16x16x32_bf16 v[8:11], v[170:173], v[194:197], v[8:11]
	v_mfma_f32_16x16x32_bf16 v[4:7], v[158:161], v[234:237], v[4:7]
	s_nop 0
	v_mfma_f32_16x16x32_bf16 v[4:7], v[162:165], v[238:241], v[4:7]
	v_mfma_f32_16x16x32_bf16 v[0:3], v[166:169], v[234:237], v[0:3]
	s_nop 0
	v_mfma_f32_16x16x32_bf16 v[0:3], v[170:173], v[238:241], v[0:3]
	s_setprio 0
	s_barrier
	s_bitcmp0_b32 s46, 0
	s_waitcnt vmcnt(15)
	v_mul_f32_e32 v128, 0x42800000, v128
	s_waitcnt vmcnt(14)
	v_mul_f32_e32 v132, 0x42800000, v132
	v_mul_f32_e32 v129, 0x42800000, v129
	v_mul_f32_e32 v133, 0x42800000, v133
	v_mul_f32_e32 v130, 0x42800000, v130
	v_mul_f32_e32 v134, 0x42800000, v134
	v_mul_f32_e32 v131, 0x42800000, v131
	v_mul_f32_e32 v135, 0x42800000, v135
	s_mov_b64 s[46:47], -1
	s_cbranch_scc0 .LBB0_350
	s_andn2_b64 vcc, exec, s[46:47]
	s_cbranch_vccnz .LBB0_346
	s_branch .LBB0_351

.LBB0_592:
	s_waitcnt lgkmcnt(0)
	s_add_i32 s4, s60, 0x180
	s_add_i32 s5, s42, 0x180
	s_barrier
	s_setprio 1
	s_waitcnt lgkmcnt(7)
	v_mfma_f32_16x16x32_bf16 v[60:63], v[164:167], v[196:199], 0
	s_waitcnt lgkmcnt(6)
	v_mfma_f32_16x16x32_bf16 v[60:63], v[160:163], v[192:195], v[60:63]
	v_mfma_f32_16x16x32_bf16 v[56:59], v[156:159], v[196:199], 0
	s_nop 0
	v_mfma_f32_16x16x32_bf16 v[56:59], v[152:155], v[192:195], v[56:59]
	s_waitcnt lgkmcnt(5)
	v_mfma_f32_16x16x32_bf16 v[52:55], v[164:167], v[188:191], 0
	s_waitcnt lgkmcnt(4)
	v_mfma_f32_16x16x32_bf16 v[52:55], v[160:163], v[184:187], v[52:55]
	v_mfma_f32_16x16x32_bf16 v[48:51], v[156:159], v[188:191], 0
	s_nop 0
	v_mfma_f32_16x16x32_bf16 v[48:51], v[152:155], v[184:187], v[48:51]
	s_waitcnt lgkmcnt(3)
	v_mfma_f32_16x16x32_bf16 v[44:47], v[164:167], v[180:183], 0
	s_waitcnt lgkmcnt(2)
	v_mfma_f32_16x16x32_bf16 v[44:47], v[160:163], v[176:179], v[44:47]
	v_mfma_f32_16x16x32_bf16 v[40:43], v[156:159], v[180:183], 0
	s_nop 0
	v_mfma_f32_16x16x32_bf16 v[40:43], v[152:155], v[176:179], v[40:43]
	s_waitcnt lgkmcnt(1)
	v_mfma_f32_16x16x32_bf16 v[36:39], v[164:167], v[172:175], 0
	s_waitcnt lgkmcnt(0)
	v_mfma_f32_16x16x32_bf16 v[36:39], v[160:163], v[168:171], v[36:39]
	v_mfma_f32_16x16x32_bf16 v[32:35], v[156:159], v[172:175], 0
	s_nop 0
	v_mfma_f32_16x16x32_bf16 v[32:35], v[152:155], v[168:171], v[32:35]
	s_setprio 0
	s_setprio 1
	v_mfma_f32_16x16x32_bf16 v[28:31], v[148:151], v[196:199], 0
	s_nop 0
	v_mfma_f32_16x16x32_bf16 v[28:31], v[144:147], v[192:195], v[28:31]
	v_mfma_f32_16x16x32_bf16 v[24:27], v[140:143], v[196:199], 0
	s_nop 0
	v_mfma_f32_16x16x32_bf16 v[24:27], v[136:139], v[192:195], v[24:27]
	v_mfma_f32_16x16x32_bf16 v[20:23], v[148:151], v[188:191], 0
	s_nop 0
	v_mfma_f32_16x16x32_bf16 v[20:23], v[144:147], v[184:187], v[20:23]
	v_mfma_f32_16x16x32_bf16 v[16:19], v[140:143], v[188:191], 0
	s_nop 0
	v_mfma_f32_16x16x32_bf16 v[16:19], v[136:139], v[184:187], v[16:19]
	v_mfma_f32_16x16x32_bf16 v[12:15], v[148:151], v[180:183], 0
	s_nop 0
	v_mfma_f32_16x16x32_bf16 v[12:15], v[144:147], v[176:179], v[12:15]
	v_mfma_f32_16x16x32_bf16 v[8:11], v[140:143], v[180:183], 0
	s_nop 0
	v_mfma_f32_16x16x32_bf16 v[8:11], v[136:139], v[176:179], v[8:11]
	v_mfma_f32_16x16x32_bf16 v[4:7], v[148:151], v[172:175], 0
	s_nop 0
	v_mfma_f32_16x16x32_bf16 v[4:7], v[144:147], v[168:171], v[4:7]
	v_mfma_f32_16x16x32_bf16 v[0:3], v[140:143], v[172:175], 0
	s_nop 0
	v_mfma_f32_16x16x32_bf16 v[0:3], v[136:139], v[168:171], v[0:3]
	s_setprio 0
	s_barrier
	ds_read_b128 v[164:167], v224
	ds_read_b128 v[160:163], v225
	ds_read_b128 v[156:159], v226
	ds_read_b128 v[152:155], v227
	ds_read_b128 v[148:151], v228
	ds_read_b128 v[144:147], v229
	ds_read_b128 v[140:143], v230
	ds_read_b128 v[136:139], v231
	ds_read_b128 v[168:171], v232 offset:32768
	ds_read_b128 v[172:175], v232 offset:33792
	ds_read_b128 v[176:179], v232 offset:34816
	ds_read_b128 v[180:183], v232 offset:35840
	ds_read_b128 v[184:187], v232 offset:36864
	ds_read_b128 v[188:191], v232 offset:37888
	ds_read_b128 v[192:195], v232 offset:38912
	ds_read_b128 v[196:199], v232 offset:39936
	s_mov_b32 m0, s68
	s_add_i32 s10, s60, 0x100100
	buffer_load_dwordx4 v213, s[12:15], s10 offen lds
	s_add_i32 s10, s60, 0x180100
	s_mov_b32 m0, s69
	s_nop 0
	buffer_load_dwordx4 v213, s[12:15], s10 offen lds
	s_waitcnt vmcnt(10)
	s_waitcnt lgkmcnt(8)
	s_barrier
	s_setprio 1
	s_waitcnt lgkmcnt(7)
	v_mfma_f32_16x16x32_bf16 v[124:127], v[164:167], v[168:171], v[124:127]
	s_waitcnt lgkmcnt(6)
	v_mfma_f32_16x16x32_bf16 v[124:127], v[160:163], v[172:175], v[124:127]
	v_mfma_f32_16x16x32_bf16 v[120:123], v[156:159], v[168:171], v[120:123]
	s_nop 0
	v_mfma_f32_16x16x32_bf16 v[120:123], v[152:155], v[172:175], v[120:123]
	s_waitcnt lgkmcnt(5)
	v_mfma_f32_16x16x32_bf16 v[116:119], v[164:167], v[176:179], v[116:119]
	s_waitcnt lgkmcnt(4)
	v_mfma_f32_16x16x32_bf16 v[116:119], v[160:163], v[180:183], v[116:119]
	v_mfma_f32_16x16x32_bf16 v[112:115], v[156:159], v[176:179], v[112:115]
	s_nop 0
	v_mfma_f32_16x16x32_bf16 v[112:115], v[152:155], v[180:183], v[112:115]
	s_waitcnt lgkmcnt(3)
	v_mfma_f32_16x16x32_bf16 v[108:111], v[164:167], v[184:187], v[108:111]
	s_waitcnt lgkmcnt(2)
	v_mfma_f32_16x16x32_bf16 v[108:111], v[160:163], v[188:191], v[108:111]
	v_mfma_f32_16x16x32_bf16 v[104:107], v[156:159], v[184:187], v[104:107]
	s_nop 0
	v_mfma_f32_16x16x32_bf16 v[104:107], v[152:155], v[188:191], v[104:107]
	s_waitcnt lgkmcnt(1)
	v_mfma_f32_16x16x32_bf16 v[100:103], v[164:167], v[192:195], v[100:103]
	s_waitcnt lgkmcnt(0)
	v_mfma_f32_16x16x32_bf16 v[100:103], v[160:163], v[196:199], v[100:103]
	v_mfma_f32_16x16x32_bf16 v[96:99], v[156:159], v[192:195], v[96:99]
	s_nop 0
	v_mfma_f32_16x16x32_bf16 v[96:99], v[152:155], v[196:199], v[96:99]
	s_setprio 0
	s_setprio 1
	v_mfma_f32_16x16x32_bf16 v[92:95], v[148:151], v[168:171], v[92:95]
	s_nop 0
	v_mfma_f32_16x16x32_bf16 v[92:95], v[144:147], v[172:175], v[92:95]
	v_mfma_f32_16x16x32_bf16 v[88:91], v[140:143], v[168:171], v[88:91]
	s_nop 0
	v_mfma_f32_16x16x32_bf16 v[88:91], v[136:139], v[172:175], v[88:91]
	v_mfma_f32_16x16x32_bf16 v[84:87], v[148:151], v[176:179], v[84:87]
	s_nop 0
	v_mfma_f32_16x16x32_bf16 v[84:87], v[144:147], v[180:183], v[84:87]
	v_mfma_f32_16x16x32_bf16 v[80:83], v[140:143], v[176:179], v[80:83]
	s_nop 0
	v_mfma_f32_16x16x32_bf16 v[80:83], v[136:139], v[180:183], v[80:83]
	v_mfma_f32_16x16x32_bf16 v[76:79], v[148:151], v[184:187], v[76:79]
	s_nop 0
	v_mfma_f32_16x16x32_bf16 v[76:79], v[144:147], v[188:191], v[76:79]
	v_mfma_f32_16x16x32_bf16 v[72:75], v[140:143], v[184:187], v[72:75]
	s_nop 0
	v_mfma_f32_16x16x32_bf16 v[72:75], v[136:139], v[188:191], v[72:75]
	v_mfma_f32_16x16x32_bf16 v[68:71], v[148:151], v[192:195], v[68:71]
	s_nop 0
	v_mfma_f32_16x16x32_bf16 v[68:71], v[144:147], v[196:199], v[68:71]
	v_mfma_f32_16x16x32_bf16 v[64:67], v[140:143], v[192:195], v[64:67]
	s_nop 0
	v_mfma_f32_16x16x32_bf16 v[64:67], v[136:139], v[196:199], v[64:67]
	s_setprio 0
	s_barrier
	ds_read_b128 v[168:171], v232 offset:49152
	ds_read_b128 v[172:175], v232 offset:50176
	ds_read_b128 v[176:179], v232 offset:51200
	ds_read_b128 v[180:183], v232 offset:52224
	ds_read_b128 v[184:187], v232 offset:53248
	ds_read_b128 v[188:191], v232 offset:54272
	ds_read_b128 v[192:195], v232 offset:55296
	ds_read_b128 v[196:199], v232 offset:56320
	s_mov_b32 m0, s72
	s_mov_b32 s10, s14
	s_mov_b32 s11, s15
	buffer_load_dwordx4 v214, s[8:11], s5 offen lds
	s_add_i32 s5, s42, 0x40180
	s_mov_b32 m0, s73
	s_nop 0
	buffer_load_dwordx4 v214, s[8:11], s5 offen lds
	s_add_i32 s5, s42, 0x4180
	s_mov_b32 m0, s76
	s_nop 0
	buffer_load_dwordx4 v214, s[8:11], s5 offen lds
	s_add_i32 s5, s42, 0x44180
	s_mov_b32 m0, s77
	s_nop 0
	buffer_load_dwordx4 v214, s[8:11], s5 offen lds
	s_mov_b32 m0, s74
	s_nop 0
	buffer_load_dwordx4 v213, s[12:15], s4 offen lds
	s_add_i32 s4, s60, 0x80180
	s_mov_b32 m0, s75
	s_nop 0
	buffer_load_dwordx4 v213, s[12:15], s4 offen lds
	s_waitcnt vmcnt(8)
	s_waitcnt lgkmcnt(6)
	s_barrier
	s_setprio 1
	s_waitcnt lgkmcnt(7)
	v_mfma_f32_16x16x32_bf16 v[60:63], v[164:167], v[168:171], v[60:63]
	s_waitcnt lgkmcnt(6)
	v_mfma_f32_16x16x32_bf16 v[60:63], v[160:163], v[172:175], v[60:63]
	v_mfma_f32_16x16x32_bf16 v[56:59], v[156:159], v[168:171], v[56:59]
	s_nop 0
	v_mfma_f32_16x16x32_bf16 v[56:59], v[152:155], v[172:175], v[56:59]
	s_waitcnt lgkmcnt(5)
	v_mfma_f32_16x16x32_bf16 v[52:55], v[164:167], v[176:179], v[52:55]
	s_waitcnt lgkmcnt(4)
	v_mfma_f32_16x16x32_bf16 v[52:55], v[160:163], v[180:183], v[52:55]
	v_mfma_f32_16x16x32_bf16 v[48:51], v[156:159], v[176:179], v[48:51]
	s_nop 0
	v_mfma_f32_16x16x32_bf16 v[48:51], v[152:155], v[180:183], v[48:51]
	s_waitcnt lgkmcnt(3)
	v_mfma_f32_16x16x32_bf16 v[44:47], v[164:167], v[184:187], v[44:47]
	s_waitcnt lgkmcnt(2)
	v_mfma_f32_16x16x32_bf16 v[44:47], v[160:163], v[188:191], v[44:47]
	v_mfma_f32_16x16x32_bf16 v[40:43], v[156:159], v[184:187], v[40:43]
	s_nop 0
	v_mfma_f32_16x16x32_bf16 v[40:43], v[152:155], v[188:191], v[40:43]
	s_waitcnt lgkmcnt(1)
	v_mfma_f32_16x16x32_bf16 v[36:39], v[164:167], v[192:195], v[36:39]
	s_waitcnt lgkmcnt(0)
	v_mfma_f32_16x16x32_bf16 v[36:39], v[160:163], v[196:199], v[36:39]
	v_mfma_f32_16x16x32_bf16 v[32:35], v[156:159], v[192:195], v[32:35]
	s_nop 0
	v_mfma_f32_16x16x32_bf16 v[32:35], v[152:155], v[196:199], v[32:35]
	s_setprio 0
	s_setprio 1
	v_mfma_f32_16x16x32_bf16 v[28:31], v[148:151], v[168:171], v[28:31]
	s_nop 0
	v_mfma_f32_16x16x32_bf16 v[28:31], v[144:147], v[172:175], v[28:31]
	v_mfma_f32_16x16x32_bf16 v[24:27], v[140:143], v[168:171], v[24:27]
	s_nop 0
	v_mfma_f32_16x16x32_bf16 v[24:27], v[136:139], v[172:175], v[24:27]
	v_mfma_f32_16x16x32_bf16 v[20:23], v[148:151], v[176:179], v[20:23]
	s_nop 0
	v_mfma_f32_16x16x32_bf16 v[20:23], v[144:147], v[180:183], v[20:23]
	v_mfma_f32_16x16x32_bf16 v[16:19], v[140:143], v[176:179], v[16:19]
	s_nop 0
	v_mfma_f32_16x16x32_bf16 v[16:19], v[136:139], v[180:183], v[16:19]
	v_mfma_f32_16x16x32_bf16 v[12:15], v[148:151], v[184:187], v[12:15]
	s_nop 0
	v_mfma_f32_16x16x32_bf16 v[12:15], v[144:147], v[188:191], v[12:15]
	v_mfma_f32_16x16x32_bf16 v[8:11], v[140:143], v[184:187], v[8:11]
	s_nop 0
	v_mfma_f32_16x16x32_bf16 v[8:11], v[136:139], v[188:191], v[8:11]
	v_mfma_f32_16x16x32_bf16 v[4:7], v[148:151], v[192:195], v[4:7]
	s_nop 0
	v_mfma_f32_16x16x32_bf16 v[4:7], v[144:147], v[196:199], v[4:7]
	v_mfma_f32_16x16x32_bf16 v[0:3], v[140:143], v[192:195], v[0:3]
	s_nop 0
	v_mfma_f32_16x16x32_bf16 v[0:3], v[136:139], v[196:199], v[0:3]
	s_setprio 0
	s_barrier
	s_waitcnt vmcnt(14)
	v_mul_f32_e32 v132, 0x42800000, v132
	v_mul_f32_e32 v128, 0x42800000, v128
	v_mul_f32_e32 v133, 0x42800000, v133
	v_mul_f32_e32 v129, 0x42800000, v129
	v_mul_f32_e32 v134, 0x42800000, v134
	v_mul_f32_e32 v130, 0x42800000, v130
	v_mul_f32_e32 v135, 0x42800000, v135
	v_mul_f32_e32 v131, 0x42800000, v131
	v_cvt_pk_fp8_f32 v202, v128, v132
	v_cvt_pk_fp8_f32 v233, v129, v133
	v_cvt_pk_fp8_f32 v234, v130, v134
	v_cvt_pk_fp8_f32 v235, v131, v135
	s_add_i32 s33, s42, 0x200
	s_mov_b32 s66, 0
	s_mov_b32 s89, s70
	s_mov_b32 s90, s71
	s_branch .LBB0_595

.LBB0_595:
	v_mov_b32_e32 v152, v202
	v_mov_b32_e32 v153, v233
	v_mov_b32_e32 v154, v234
	v_mov_b32_e32 v155, v235
	ds_read_b128 v[158:161], v216
	ds_read_b128 v[162:165], v217
	ds_read_b128 v[166:169], v218
	ds_read_b128 v[170:173], v219
	ds_read_b128 v[148:151], v220
	ds_read_b128 v[144:147], v221
	ds_read_b128 v[140:143], v222
	ds_read_b128 v[136:139], v223
	ds_read_b128 v[174:177], v232
	ds_read_b128 v[178:181], v232 offset:1024
	ds_read_b128 v[182:185], v232 offset:2048
	ds_read_b128 v[186:189], v232 offset:3072
	ds_read_b128 v[190:193], v232 offset:4096
	ds_read_b128 v[194:197], v232 offset:5120
	ds_read_b128 v[234:237], v232 offset:6144
	ds_read_b128 v[238:241], v232 offset:7168
	s_add_i32 s4, s60, s66
	s_mov_b32 s42, s90
	s_add_i32 s90, s90, 1
	s_add_i32 s5, s4, 0x200
	s_add_i32 s67, s33, s66
	s_cmpk_eq_i32 s66, 0x200
	s_cselect_b32 s43, s87, s5
	s_cselect_b32 s93, s88, s67
	s_add_i32 s92, s43, 0x80
	s_mov_b32 m0, s78
	s_add_i32 s5, s4, 0x100180
	buffer_load_dwordx4 v213, s[12:15], s5 offen lds
	s_add_i32 s4, s4, 0x180180
	s_mov_b32 m0, s81
	s_add_i32 s94, s93, 0x80
	buffer_load_dwordx4 v213, s[12:15], s4 offen lds
	s_lshr_b32 s4, s90, 2
	s_mul_i32 s67, s4, s34
	s_add_i32 s67, s67, s2
	s_cmp_lt_i32 s4, s3
	s_cselect_b64 s[4:5], -1, 0
	s_and_b64 s[96:97], s[4:5], exec
	s_cselect_b32 s91, s67, 0
	s_ashr_i32 s96, s91, 7
	s_bfe_u32 s95, s90, 0x10001
	s_ashr_i32 s97, s96, 31
	s_or_b32 s95, s95, s79
	s_lshl_b64 s[96:97], s[96:97], 23
	s_add_u32 s96, s48, s96
	s_addc_u32 s97, s49, s97
	s_lshl_b32 vcc_lo, s91, 16
	s_and_b32 vcc_lo, vcc_lo, 0x600000
	s_add_u32 s96, s96, vcc_lo
	s_addc_u32 s97, s97, 0
	s_lshl_b32 s91, s91, 7
	s_and_b32 s91, s91, 0xf80
	s_lshl_b32 vcc_lo, s91, 2
	s_add_u32 s96, s96, vcc_lo
	v_and_or_b32 v202, s89, 2, v200
	s_addc_u32 s97, s97, 0
	v_lshl_or_b32 v156, s95, 5, v215
	v_lshlrev_b64 v[128:129], 14, v[202:203]
	v_lshl_add_u64 v[128:129], s[96:97], 0, v[128:129]
	v_lshlrev_b32_e32 v202, 2, v156
	v_lshl_add_u64 v[128:129], v[128:129], 0, v[202:203]
	s_movk_i32 s95, 0x4000
	v_add_co_u32_e32 v132, vcc, s95, v128
	s_nop 1
	v_addc_co_u32_e32 v133, vcc, 0, v129, vcc
	global_load_dwordx4 v[128:131], v[128:129], off nt
	s_nop 0
	global_load_dwordx4 v[132:135], v[132:133], off nt
	s_waitcnt vmcnt(10)
	s_waitcnt lgkmcnt(8)
	s_barrier
	s_setprio 1
	s_waitcnt lgkmcnt(7)
	v_mfma_f32_16x16x32_bf16 v[124:127], v[158:161], v[174:177], v[124:127]
	s_waitcnt lgkmcnt(6)
	v_mfma_f32_16x16x32_bf16 v[124:127], v[162:165], v[178:181], v[124:127]
	v_mfma_f32_16x16x32_bf16 v[120:123], v[166:169], v[174:177], v[120:123]
	s_nop 0
	v_mfma_f32_16x16x32_bf16 v[120:123], v[170:173], v[178:181], v[120:123]
	s_waitcnt lgkmcnt(5)
	v_mfma_f32_16x16x32_bf16 v[116:119], v[158:161], v[182:185], v[116:119]
	s_waitcnt lgkmcnt(4)
	v_mfma_f32_16x16x32_bf16 v[116:119], v[162:165], v[186:189], v[116:119]
	v_mfma_f32_16x16x32_bf16 v[112:115], v[166:169], v[182:185], v[112:115]
	s_nop 0
	v_mfma_f32_16x16x32_bf16 v[112:115], v[170:173], v[186:189], v[112:115]
	s_waitcnt lgkmcnt(3)
	v_mfma_f32_16x16x32_bf16 v[108:111], v[158:161], v[190:193], v[108:111]
	s_waitcnt lgkmcnt(2)
	v_mfma_f32_16x16x32_bf16 v[108:111], v[162:165], v[194:197], v[108:111]
	v_mfma_f32_16x16x32_bf16 v[104:107], v[166:169], v[190:193], v[104:107]
	s_nop 0
	v_mfma_f32_16x16x32_bf16 v[104:107], v[170:173], v[194:197], v[104:107]
	s_waitcnt lgkmcnt(1)
	v_mfma_f32_16x16x32_bf16 v[100:103], v[158:161], v[234:237], v[100:103]
	s_waitcnt lgkmcnt(0)
	v_mfma_f32_16x16x32_bf16 v[100:103], v[162:165], v[238:241], v[100:103]
	v_mfma_f32_16x16x32_bf16 v[96:99], v[166:169], v[234:237], v[96:99]
	s_nop 0
	v_mfma_f32_16x16x32_bf16 v[96:99], v[170:173], v[238:241], v[96:99]
	s_setprio 0
	s_setprio 1
	v_mfma_f32_16x16x32_bf16 v[92:95], v[148:151], v[174:177], v[92:95]
	s_nop 0
	v_mfma_f32_16x16x32_bf16 v[92:95], v[144:147], v[178:181], v[92:95]
	v_mfma_f32_16x16x32_bf16 v[88:91], v[140:143], v[174:177], v[88:91]
	s_nop 0
	v_mfma_f32_16x16x32_bf16 v[88:91], v[136:139], v[178:181], v[88:91]
	v_mfma_f32_16x16x32_bf16 v[84:87], v[148:151], v[182:185], v[84:87]
	s_nop 0
	v_mfma_f32_16x16x32_bf16 v[84:87], v[144:147], v[186:189], v[84:87]
	v_mfma_f32_16x16x32_bf16 v[80:83], v[140:143], v[182:185], v[80:83]
	s_nop 0
	v_mfma_f32_16x16x32_bf16 v[80:83], v[136:139], v[186:189], v[80:83]
	v_mfma_f32_16x16x32_bf16 v[76:79], v[148:151], v[190:193], v[76:79]
	s_nop 0
	v_mfma_f32_16x16x32_bf16 v[76:79], v[144:147], v[194:197], v[76:79]
	v_mfma_f32_16x16x32_bf16 v[72:75], v[140:143], v[190:193], v[72:75]
	s_nop 0
	v_mfma_f32_16x16x32_bf16 v[72:75], v[136:139], v[194:197], v[72:75]
	v_mfma_f32_16x16x32_bf16 v[68:71], v[148:151], v[234:237], v[68:71]
	s_nop 0
	v_mfma_f32_16x16x32_bf16 v[68:71], v[144:147], v[238:241], v[68:71]
	v_mfma_f32_16x16x32_bf16 v[64:67], v[140:143], v[234:237], v[64:67]
	s_nop 0
	v_mfma_f32_16x16x32_bf16 v[64:67], v[136:139], v[238:241], v[64:67]
	s_setprio 0
	s_barrier
	ds_read_b128 v[174:177], v232 offset:16384
	ds_read_b128 v[178:181], v232 offset:17408
	ds_read_b128 v[182:185], v232 offset:18432
	ds_read_b128 v[186:189], v232 offset:19456
	ds_read_b128 v[190:193], v232 offset:20480
	ds_read_b128 v[194:197], v232 offset:21504
	ds_read_b128 v[234:237], v232 offset:22528
	ds_read_b128 v[238:241], v232 offset:23552
	s_mov_b32 m0, s47
	s_add_i32 s95, s93, 0x40000
	buffer_load_dwordx4 v214, s[8:11], s93 offen lds
	s_mov_b32 m0, s62
	s_nop 0
	buffer_load_dwordx4 v214, s[8:11], s95 offen lds
	s_add_i32 s95, s93, 0x4000
	s_mov_b32 m0, s63
	s_nop 0
	buffer_load_dwordx4 v214, s[8:11], s95 offen lds
	s_add_i32 s95, s93, 0x44000
	s_mov_b32 m0, s64
	s_nop 0
	buffer_load_dwordx4 v214, s[8:11], s95 offen lds
	s_mov_b32 m0, s46
	s_add_i32 s95, s43, 0x80000
	buffer_load_dwordx4 v213, s[12:15], s43 offen lds
	s_mov_b32 m0, s65
	s_nop 0
	buffer_load_dwordx4 v213, s[12:15], s95 offen lds
	s_waitcnt vmcnt(10)
	s_waitcnt lgkmcnt(6)
	s_barrier
	s_setprio 1
	s_waitcnt lgkmcnt(7)
	v_mfma_f32_16x16x32_bf16 v[60:63], v[158:161], v[174:177], v[60:63]
	s_waitcnt lgkmcnt(6)
	v_mfma_f32_16x16x32_bf16 v[60:63], v[162:165], v[178:181], v[60:63]
	v_mfma_f32_16x16x32_bf16 v[56:59], v[166:169], v[174:177], v[56:59]
	s_nop 0
	v_mfma_f32_16x16x32_bf16 v[56:59], v[170:173], v[178:181], v[56:59]
	s_waitcnt lgkmcnt(5)
	v_mfma_f32_16x16x32_bf16 v[52:55], v[158:161], v[182:185], v[52:55]
	s_waitcnt lgkmcnt(4)
	v_mfma_f32_16x16x32_bf16 v[52:55], v[162:165], v[186:189], v[52:55]
	v_mfma_f32_16x16x32_bf16 v[48:51], v[166:169], v[182:185], v[48:51]
	s_nop 0
	v_mfma_f32_16x16x32_bf16 v[48:51], v[170:173], v[186:189], v[48:51]
	s_waitcnt lgkmcnt(3)
	v_mfma_f32_16x16x32_bf16 v[44:47], v[158:161], v[190:193], v[44:47]
	s_waitcnt lgkmcnt(2)
	v_mfma_f32_16x16x32_bf16 v[44:47], v[162:165], v[194:197], v[44:47]
	v_mfma_f32_16x16x32_bf16 v[40:43], v[166:169], v[190:193], v[40:43]
	s_nop 0
	v_mfma_f32_16x16x32_bf16 v[40:43], v[170:173], v[194:197], v[40:43]
	s_waitcnt lgkmcnt(1)
	v_mfma_f32_16x16x32_bf16 v[36:39], v[158:161], v[234:237], v[36:39]
	s_waitcnt lgkmcnt(0)
	v_mfma_f32_16x16x32_bf16 v[36:39], v[162:165], v[238:241], v[36:39]
	v_mfma_f32_16x16x32_bf16 v[32:35], v[166:169], v[234:237], v[32:35]
	s_nop 0
	v_mfma_f32_16x16x32_bf16 v[32:35], v[170:173], v[238:241], v[32:35]
	s_setprio 0
	s_setprio 1
	v_mfma_f32_16x16x32_bf16 v[28:31], v[148:151], v[174:177], v[28:31]
	s_nop 0
	v_mfma_f32_16x16x32_bf16 v[28:31], v[144:147], v[178:181], v[28:31]
	v_mfma_f32_16x16x32_bf16 v[24:27], v[140:143], v[174:177], v[24:27]
	s_nop 0
	v_mfma_f32_16x16x32_bf16 v[24:27], v[136:139], v[178:181], v[24:27]
	v_mfma_f32_16x16x32_bf16 v[20:23], v[148:151], v[182:185], v[20:23]
	s_nop 0
	v_mfma_f32_16x16x32_bf16 v[20:23], v[144:147], v[186:189], v[20:23]
	v_mfma_f32_16x16x32_bf16 v[16:19], v[140:143], v[182:185], v[16:19]
	s_nop 0
	v_mfma_f32_16x16x32_bf16 v[16:19], v[136:139], v[186:189], v[16:19]
	v_mfma_f32_16x16x32_bf16 v[12:15], v[148:151], v[190:193], v[12:15]
	s_nop 0
	v_mfma_f32_16x16x32_bf16 v[12:15], v[144:147], v[194:197], v[12:15]
	v_mfma_f32_16x16x32_bf16 v[8:11], v[140:143], v[190:193], v[8:11]
	s_nop 0
	v_mfma_f32_16x16x32_bf16 v[8:11], v[136:139], v[194:197], v[8:11]
	v_mfma_f32_16x16x32_bf16 v[4:7], v[148:151], v[234:237], v[4:7]
	s_nop 0
	v_mfma_f32_16x16x32_bf16 v[4:7], v[144:147], v[238:241], v[4:7]
	v_mfma_f32_16x16x32_bf16 v[0:3], v[140:143], v[234:237], v[0:3]
	s_nop 0
	v_mfma_f32_16x16x32_bf16 v[0:3], v[136:139], v[238:241], v[0:3]
	s_setprio 0
	s_barrier
	ds_read_b128 v[136:139], v224
	ds_read_b128 v[140:143], v225
	ds_read_b128 v[144:147], v226
	ds_read_b128 v[148:151], v227
	ds_read_b128 v[158:161], v228
	ds_read_b128 v[162:165], v229
	ds_read_b128 v[166:169], v230
	ds_read_b128 v[170:173], v231
	ds_read_b128 v[174:177], v232 offset:32768
	ds_read_b128 v[178:181], v232 offset:33792
	ds_read_b128 v[182:185], v232 offset:34816
	ds_read_b128 v[186:189], v232 offset:35840
	ds_read_b128 v[190:193], v232 offset:36864
	ds_read_b128 v[194:197], v232 offset:37888
	ds_read_b128 v[234:237], v232 offset:38912
	ds_read_b128 v[238:241], v232 offset:39936
	s_mov_b32 m0, s68
	s_add_i32 s95, s43, 0x100000
	buffer_load_dwordx4 v213, s[12:15], s95 offen lds
	s_add_i32 s95, s43, 0x180000
	s_mov_b32 m0, s69
	s_nop 0
	buffer_load_dwordx4 v213, s[12:15], s95 offen lds
	s_waitcnt vmcnt(10)
	s_waitcnt lgkmcnt(8)
	s_barrier
	s_setprio 1
	s_waitcnt lgkmcnt(7)
	v_mfma_f32_16x16x32_bf16 v[124:127], v[136:139], v[174:177], v[124:127]
	s_waitcnt lgkmcnt(6)
	v_mfma_f32_16x16x32_bf16 v[124:127], v[140:143], v[178:181], v[124:127]
	v_mfma_f32_16x16x32_bf16 v[120:123], v[144:147], v[174:177], v[120:123]
	s_nop 0
	v_mfma_f32_16x16x32_bf16 v[120:123], v[148:151], v[178:181], v[120:123]
	s_waitcnt lgkmcnt(5)
	v_mfma_f32_16x16x32_bf16 v[116:119], v[136:139], v[182:185], v[116:119]
	s_waitcnt lgkmcnt(4)
	v_mfma_f32_16x16x32_bf16 v[116:119], v[140:143], v[186:189], v[116:119]
	v_mfma_f32_16x16x32_bf16 v[112:115], v[144:147], v[182:185], v[112:115]
	s_nop 0
	v_mfma_f32_16x16x32_bf16 v[112:115], v[148:151], v[186:189], v[112:115]
	s_waitcnt lgkmcnt(3)
	v_mfma_f32_16x16x32_bf16 v[108:111], v[136:139], v[190:193], v[108:111]
	s_waitcnt lgkmcnt(2)
	v_mfma_f32_16x16x32_bf16 v[108:111], v[140:143], v[194:197], v[108:111]
	v_mfma_f32_16x16x32_bf16 v[104:107], v[144:147], v[190:193], v[104:107]
	s_nop 0
	v_mfma_f32_16x16x32_bf16 v[104:107], v[148:151], v[194:197], v[104:107]
	s_waitcnt lgkmcnt(1)
	v_mfma_f32_16x16x32_bf16 v[100:103], v[136:139], v[234:237], v[100:103]
	s_waitcnt lgkmcnt(0)
	v_mfma_f32_16x16x32_bf16 v[100:103], v[140:143], v[238:241], v[100:103]
	v_mfma_f32_16x16x32_bf16 v[96:99], v[144:147], v[234:237], v[96:99]
	s_nop 0
	v_mfma_f32_16x16x32_bf16 v[96:99], v[148:151], v[238:241], v[96:99]
	s_setprio 0
	s_setprio 1
	v_mfma_f32_16x16x32_bf16 v[92:95], v[158:161], v[174:177], v[92:95]
	s_nop 0
	v_mfma_f32_16x16x32_bf16 v[92:95], v[162:165], v[178:181], v[92:95]
	v_mfma_f32_16x16x32_bf16 v[88:91], v[166:169], v[174:177], v[88:91]
	s_nop 0
	v_mfma_f32_16x16x32_bf16 v[88:91], v[170:173], v[178:181], v[88:91]
	v_mfma_f32_16x16x32_bf16 v[84:87], v[158:161], v[182:185], v[84:87]
	s_nop 0
	v_mfma_f32_16x16x32_bf16 v[84:87], v[162:165], v[186:189], v[84:87]
	v_mfma_f32_16x16x32_bf16 v[80:83], v[166:169], v[182:185], v[80:83]
	s_nop 0
	v_mfma_f32_16x16x32_bf16 v[80:83], v[170:173], v[186:189], v[80:83]
	v_mfma_f32_16x16x32_bf16 v[76:79], v[158:161], v[190:193], v[76:79]
	s_nop 0
	v_mfma_f32_16x16x32_bf16 v[76:79], v[162:165], v[194:197], v[76:79]
	v_mfma_f32_16x16x32_bf16 v[72:75], v[166:169], v[190:193], v[72:75]
	s_nop 0
	v_mfma_f32_16x16x32_bf16 v[72:75], v[170:173], v[194:197], v[72:75]
	v_mfma_f32_16x16x32_bf16 v[68:71], v[158:161], v[234:237], v[68:71]
	s_nop 0
	v_mfma_f32_16x16x32_bf16 v[68:71], v[162:165], v[238:241], v[68:71]
	v_mfma_f32_16x16x32_bf16 v[64:67], v[166:169], v[234:237], v[64:67]
	s_nop 0
	v_mfma_f32_16x16x32_bf16 v[64:67], v[170:173], v[238:241], v[64:67]
	s_setprio 0
	s_barrier
	ds_read_b128 v[174:177], v232 offset:49152
	ds_read_b128 v[178:181], v232 offset:50176
	ds_read_b128 v[182:185], v232 offset:51200
	ds_read_b128 v[186:189], v232 offset:52224
	ds_read_b128 v[190:193], v232 offset:53248
	ds_read_b128 v[194:197], v232 offset:54272
	ds_read_b128 v[234:237], v232 offset:55296
	ds_read_b128 v[238:241], v232 offset:56320
	s_mov_b32 m0, s72
	s_add_i32 s43, s43, 0x80080
	buffer_load_dwordx4 v214, s[8:11], s94 offen lds
	s_add_i32 s94, s93, 0x40080
	s_mov_b32 m0, s73
	s_nop 0
	buffer_load_dwordx4 v214, s[8:11], s94 offen lds
	s_add_i32 s94, s93, 0x4080
	s_mov_b32 m0, s76
	s_add_i32 s93, s93, 0x44080
	buffer_load_dwordx4 v214, s[8:11], s94 offen lds
	s_mov_b32 m0, s77
	s_nop 0
	buffer_load_dwordx4 v214, s[8:11], s93 offen lds
	s_mov_b32 m0, s74
	s_nop 0
	buffer_load_dwordx4 v213, s[12:15], s92 offen lds
	s_mov_b32 m0, s75
	s_nop 0
	buffer_load_dwordx4 v213, s[12:15], s43 offen lds
	s_waitcnt vmcnt(8)
	s_waitcnt lgkmcnt(6)
	s_barrier
	s_setprio 1
	s_waitcnt lgkmcnt(7)
	v_mfma_f32_16x16x32_bf16 v[60:63], v[136:139], v[174:177], v[60:63]
	s_waitcnt lgkmcnt(6)
	v_mfma_f32_16x16x32_bf16 v[60:63], v[140:143], v[178:181], v[60:63]
	v_mfma_f32_16x16x32_bf16 v[56:59], v[144:147], v[174:177], v[56:59]
	s_nop 0
	v_mfma_f32_16x16x32_bf16 v[56:59], v[148:151], v[178:181], v[56:59]
	s_waitcnt lgkmcnt(5)
	v_mfma_f32_16x16x32_bf16 v[52:55], v[136:139], v[182:185], v[52:55]
	s_waitcnt lgkmcnt(4)
	v_mfma_f32_16x16x32_bf16 v[52:55], v[140:143], v[186:189], v[52:55]
	v_mfma_f32_16x16x32_bf16 v[48:51], v[144:147], v[182:185], v[48:51]
	s_nop 0
	v_mfma_f32_16x16x32_bf16 v[48:51], v[148:151], v[186:189], v[48:51]
	s_waitcnt lgkmcnt(3)
	v_mfma_f32_16x16x32_bf16 v[44:47], v[136:139], v[190:193], v[44:47]
	s_waitcnt lgkmcnt(2)
	v_mfma_f32_16x16x32_bf16 v[44:47], v[140:143], v[194:197], v[44:47]
	v_mfma_f32_16x16x32_bf16 v[40:43], v[144:147], v[190:193], v[40:43]
	s_nop 0
	v_mfma_f32_16x16x32_bf16 v[40:43], v[148:151], v[194:197], v[40:43]
	s_waitcnt lgkmcnt(1)
	v_mfma_f32_16x16x32_bf16 v[36:39], v[136:139], v[234:237], v[36:39]
	s_waitcnt lgkmcnt(0)
	v_mfma_f32_16x16x32_bf16 v[36:39], v[140:143], v[238:241], v[36:39]
	v_mfma_f32_16x16x32_bf16 v[32:35], v[144:147], v[234:237], v[32:35]
	s_nop 0
	v_mfma_f32_16x16x32_bf16 v[32:35], v[148:151], v[238:241], v[32:35]
	s_setprio 0
	s_setprio 1
	v_mfma_f32_16x16x32_bf16 v[28:31], v[158:161], v[174:177], v[28:31]
	s_nop 0
	v_mfma_f32_16x16x32_bf16 v[28:31], v[162:165], v[178:181], v[28:31]
	v_mfma_f32_16x16x32_bf16 v[24:27], v[166:169], v[174:177], v[24:27]
	s_nop 0
	v_mfma_f32_16x16x32_bf16 v[24:27], v[170:173], v[178:181], v[24:27]
	v_mfma_f32_16x16x32_bf16 v[20:23], v[158:161], v[182:185], v[20:23]
	s_nop 0
	v_mfma_f32_16x16x32_bf16 v[20:23], v[162:165], v[186:189], v[20:23]
	v_mfma_f32_16x16x32_bf16 v[16:19], v[166:169], v[182:185], v[16:19]
	s_nop 0
	v_mfma_f32_16x16x32_bf16 v[16:19], v[170:173], v[186:189], v[16:19]
	v_mfma_f32_16x16x32_bf16 v[12:15], v[158:161], v[190:193], v[12:15]
	s_nop 0
	v_mfma_f32_16x16x32_bf16 v[12:15], v[162:165], v[194:197], v[12:15]
	v_mfma_f32_16x16x32_bf16 v[8:11], v[166:169], v[190:193], v[8:11]
	s_nop 0
	v_mfma_f32_16x16x32_bf16 v[8:11], v[170:173], v[194:197], v[8:11]
	v_mfma_f32_16x16x32_bf16 v[4:7], v[158:161], v[234:237], v[4:7]
	s_nop 0
	v_mfma_f32_16x16x32_bf16 v[4:7], v[162:165], v[238:241], v[4:7]
	v_mfma_f32_16x16x32_bf16 v[0:3], v[166:169], v[234:237], v[0:3]
	s_nop 0
	v_mfma_f32_16x16x32_bf16 v[0:3], v[170:173], v[238:241], v[0:3]
	s_setprio 0
	s_barrier
	s_bitcmp0_b32 s42, 0
	s_waitcnt vmcnt(15)
	v_mul_f32_e32 v128, 0x42800000, v128
	s_waitcnt vmcnt(14)
	v_mul_f32_e32 v132, 0x42800000, v132
	v_mul_f32_e32 v129, 0x42800000, v129
	v_mul_f32_e32 v133, 0x42800000, v133
	v_mul_f32_e32 v130, 0x42800000, v130
	v_mul_f32_e32 v134, 0x42800000, v134
	v_mul_f32_e32 v131, 0x42800000, v131
	v_mul_f32_e32 v135, 0x42800000, v135
	s_mov_b64 s[42:43], -1
	s_cbranch_scc0 .LBB0_598
	s_andn2_b64 vcc, exec, s[42:43]
	s_cbranch_vccnz .LBB0_594
	s_branch .LBB0_599
